# every wave only stages its last two tiles; waves 0-3 store their own and their SIMD partner's staged pass while waiting at barrier 1 (LDS flag)
# speedup vs baseline: 1.0332x; 1.0233x over previous
.LBB1_12:
	s_ashr_i32 s0, s2, 2
	s_and_b32 s27, s2, 7
	s_and_b32 s28, s0, -2
	s_lshl_b32 s1, s28, 11
	s_lshl_b32 s12, s27, 17
	s_add_i32 s1, s1, s12
	v_lshlrev_b32_e32 v6, 2, v0
	v_or_b32_e32 v2, s1, v6
	v_lshlrev_b32_e32 v2, 2, v2
	global_load_dwordx4 v[2:5], v2, s[4:5]
	s_lshr_b32 s22, s19, 6
	s_lshl_b32 s29, s22, 3
	s_lshl_b32 s13, s0, 11
	s_add_i32 s0, s29, s0
	s_and_b32 s0, s0, 62
	v_and_b32_e32 v42, 63, v0
	s_lshl_b32 s14, s27, 18
	s_lshl_b32 s0, s0, 12
	v_lshrrev_b32_e32 v43, 4, v0
	v_lshlrev_b32_e32 v230, 4, v0
	v_lshlrev_b32_e32 v231, 4, v42
	s_or_b32 s0, s14, s0
	v_mov_b32_e32 v39, 0
	v_mul_u32_u24_e32 v7, 0x44, v43
	v_and_b32_e32 v44, 0xf0, v230
	s_bitset1_b32 s13, 11
	v_or_b32_e32 v6, s12, v6
	v_or_b32_e32 v38, s0, v231
	s_movk_i32 s1, 0x1000
	v_lshl_add_u32 v45, v7, 2, v44
	v_add_lshl_u32 v46, v6, s13, 2
	v_lshl_add_u64 v[6:7], s[6:7], 0, v[38:39]
	v_add_u32_e32 v232, 0x24200, v45
	v_add_co_u32_e32 v40, vcc, s1, v6
	v_max_f32_e64 v35, |v35|, |v35|
	s_nop 0
	v_addc_co_u32_e32 v41, vcc, 0, v7, vcc
	v_max_f32_e64 v1, |v1|, |v1|
	v_max_f32_e32 v1, v1, v35
	s_brev_b32 s12, -2
	v_mov_b32_e32 v39, s3
	v_bfi_b32 v37, s12, v37, v39
	s_mov_b32 s12, 0
	v_readfirstlane_b32 s18, v37
	v_and_b32_e32 v35, 31, v0
	s_waitcnt vmcnt(0)
	s_lshr_b32 s74, s19, 4
	s_and_b32 s74, s74, 12
	s_add_i32 s74, s74, 0x26c00
	v_mov_b32_e32 v250, s74
	v_mov_b32_e32 v251, 0
	ds_write_b32 v250, v251
	ds_write_b128 v232, v[2:5]
	s_waitcnt lgkmcnt(0)
	s_barrier
	global_load_dwordx4 v[128:131], v46, s[4:5]
	v_div_scale_f32 v40, s[0:1], v1, v1, v36
	v_rcp_f32_e32 v41, v40
	v_bfe_u32 v38, v0, 5, 1
	v_fma_f32 v37, -v40, v41, 1.0
	v_fmac_f32_e32 v41, v37, v41
	v_div_scale_f32 v37, vcc, v36, v1, v36
	v_mul_f32_e32 v39, v37, v41
	v_fma_f32 v46, -v40, v39, v37
	v_fmac_f32_e32 v39, v46, v41
	v_fma_f32 v37, -v40, v39, v37
	v_div_fmas_f32 v37, v37, v41, v39
	v_div_scale_f32 v39, s[0:1], v1, v1, v34
	v_rcp_f32_e32 v40, v39
	v_div_fixup_f32 v36, v37, v1, v36
	v_cmp_lt_f32_e64 s[0:1], 0, v1
	v_fma_f32 v37, -v39, v40, 1.0
	v_fmac_f32_e32 v40, v37, v40
	v_div_scale_f32 v37, vcc, v34, v1, v34
	v_mul_f32_e32 v41, v37, v40
	v_fma_f32 v46, -v39, v41, v37
	v_fmac_f32_e32 v41, v46, v40
	v_fma_f32 v37, -v39, v41, v37
	v_div_fmas_f32 v37, v37, v40, v41
	v_div_fixup_f32 v34, v37, v1, v34
	v_cndmask_b32_e64 v36, 0, v36, s[0:1]
	v_cndmask_b32_e64 v34, 0, v34, s[0:1]
	s_lshl_b32 s0, s2, 16
	s_and_b32 s1, s19, 0xffffffc0
	v_bfe_u32 v37, v0, 2, 1
	v_and_b32_e32 v39, 3, v0
	v_lshrrev_b32_e32 v40, 1, v0
	v_readfirstlane_b32 s30, v36
	s_add_i32 s0, s1, s0
	v_and_or_b32 v39, v40, 12, v39
	v_cmp_eq_u32_e32 vcc, v37, v38
	s_mov_b32 s14, s12
	s_mov_b32 s15, s12
	s_mov_b32 s13, s12
	v_mov_b64_e32 v[48:49], s[14:15]
	v_mov_b32_e32 v36, s0
	v_mov_b64_e32 v[46:47], s[12:13]
	v_readfirstlane_b32 s14, v1
	v_readfirstlane_b32 s13, v34
	v_cndmask_b32_e32 v233, 16, v39, vcc
	v_mbcnt_lo_u32_b32 v34, -1, 0
	v_mbcnt_hi_u32_b32 v34, -1, v34
	v_and_b32_e32 v40, 64, v34
	v_xor_b32_e32 v39, 32, v34
	v_add_u32_e32 v40, 64, v40
	v_cmp_lt_i32_e32 vcc, v39, v40
	s_cmp_lt_u32 s19, 64
	v_mul_u32_u24_e32 v1, 0x44, v35
	v_cndmask_b32_e32 v34, v34, v39, vcc
	v_lshlrev_b32_e32 v234, 2, v34
	v_lshlrev_b32_e32 v34, 2, v35
	s_cselect_b64 s[2:3], -1, 0
	s_cmp_gt_u32 s19, 63
	s_mul_i32 s19, s22, 0x2200
	v_lshlrev_b32_e32 v1, 2, v1
	v_or_b32_e32 v235, 0x26400, v34
	v_or_b32_e32 v236, 0x26800, v34
	s_cselect_b64 s[20:21], -1, 0
	v_lshlrev_b32_e32 v34, 4, v38
	s_lshl_b32 s15, s22, 15
	s_add_i32 s19, s19, 0x13200
	v_add_u32_e32 v36, 0x24200, v1
	v_and_b32_e32 v37, 32, v0
	v_add_u32_e32 v39, 0x11000, v1
	s_or_b32 s33, s15, 0x2000
	s_or_b32 s34, s15, 0x3000
	s_or_b32 s35, s15, 0x4000
	s_or_b32 s36, s15, 0x5000
	s_or_b32 s37, s15, 0x6000
	s_or_b32 s38, s15, 0x7000
	v_lshl_or_b32 v35, s22, 5, v35
	s_movk_i32 s15, 0x110
	v_add3_u32 v238, s19, v1, v34
	v_bfe_u32 v239, v0, 4, 2
	v_and_b32_e32 v1, 15, v0
	v_mov_b32_e32 v38, s19
	v_bfe_u32 v0, v0, 3, 1
	v_mad_u64_u32 v[164:165], s[24:25], v35, s15, v[34:35]
	v_lshlrev_b32_e32 v35, 2, v43
	v_mad_u32_u24 v38, v239, s15, v38
	v_lshlrev_b32_e32 v1, 4, v1
	v_or_b32_e32 v241, s29, v0
	v_mul_u32_u24_e32 v0, 0x110, v43
	v_cmp_gt_u32_e64 s[0:1], 32, v42
	s_lshl_b32 s31, s22, 7
	v_or_b32_e32 v165, 0x26400, v35
	v_add_u32_e32 v237, 0x11000, v45
	s_add_i32 s39, s29, s28
	v_and_b32_e32 v240, 0x70, v230
	v_or_b32_e32 v242, 0x26800, v35
	s_mov_b32 s19, s18
	s_mov_b32 s15, s14
	s_mov_b32 s40, s30
	s_mov_b32 s41, s30
	s_mov_b32 s42, s30
	s_mov_b32 s43, s30
	s_mov_b32 s44, s30
	s_mov_b32 s45, s30
	s_mov_b32 s46, s30
	s_mov_b32 s47, s13
	s_mov_b32 s48, s13
	s_mov_b32 s49, s13
	s_mov_b32 s50, s13
	s_mov_b32 s51, s13
	s_mov_b32 s52, s13
	s_mov_b32 s53, s13
	v_add_u32_e32 v243, v36, v37
	s_mov_b32 s22, 0x3e38aa3b
	v_add_u32_e32 v244, v39, v34
	v_add_u32_e32 v245, v44, v0
	s_movk_i32 s54, 0x1f80
	v_add_u32_e32 v246, v38, v1
	s_mov_b32 s57, s12
	s_add_i32 s62, s28, s29
	s_lshl_b32 s62, s62, 12
	s_lshl_b32 s66, s27, 18
	s_and_b32 s63, s62, 0x3f000
	s_or_b32 s63, s63, s66
	v_or_b32_e32 v2, s63, v231
	global_load_dwordx4 v[48:51], v2, s[6:7]
	global_load_dwordx4 v[52:55], v2, s[6:7] offset:1024
	global_load_dwordx4 v[56:59], v2, s[6:7] offset:2048
	global_load_dwordx4 v[60:63], v2, s[6:7] offset:3072
	s_add_i32 s63, s62, 0x4000
	s_and_b32 s63, s63, 0x3f000
	s_or_b32 s63, s63, s66
	v_or_b32_e32 v3, s63, v231
	global_load_dwordx4 v[40:43], v3, s[6:7] offset:2048
	global_load_dwordx4 v[44:47], v3, s[6:7] offset:3072
	s_add_i32 s63, s62, 0x6000
	s_and_b32 s63, s63, 0x3f000
	s_or_b32 s63, s63, s66
	v_or_b32_e32 v2, s63, v231
	global_load_dwordx4 v[148:151], v2, s[6:7] offset:3072
	s_add_i32 s63, s62, 0x7000
	s_and_b32 s63, s63, 0x3f000
	s_or_b32 s63, s63, s66
	v_or_b32_e32 v3, s63, v231
	global_load_dwordx4 v[132:135], v3, s[6:7]
	global_load_dwordx4 v[136:139], v3, s[6:7] offset:1024
	global_load_dwordx4 v[140:143], v3, s[6:7] offset:2048
	global_load_dwordx4 v[144:147], v3, s[6:7] offset:3072
	s_add_i32 s63, s62, 0x1000
	s_and_b32 s63, s63, 0x3f000
	s_or_b32 s63, s63, s66
	v_or_b32_e32 v2, s63, v231
	global_load_dwordx4 v[152:155], v2, s[6:7]
	global_load_dwordx4 v[156:159], v2, s[6:7] offset:1024
	s_add_i32 s63, s62, 0x4000
	s_and_b32 s63, s63, 0x3f000
	s_or_b32 s63, s63, s66
	v_or_b32_e32 v3, s63, v231
	global_load_dwordx4 v[32:35], v3, s[6:7]
	global_load_dwordx4 v[36:39], v3, s[6:7] offset:1024
	s_add_i32 s63, s62, 0x5000
	s_and_b32 s63, s63, 0x3f000
	s_or_b32 s63, s63, s66
	v_or_b32_e32 v2, s63, v231
	global_load_dwordx4 v[16:19], v2, s[6:7]
	global_load_dwordx4 v[20:23], v2, s[6:7] offset:1024
	global_load_dwordx4 v[24:27], v2, s[6:7] offset:2048
	global_load_dwordx4 v[28:31], v2, s[6:7] offset:3072
	s_add_i32 s63, s62, 0x6000
	s_and_b32 s63, s63, 0x3f000
	s_or_b32 s63, s63, s66
	v_or_b32_e32 v3, s63, v231
	global_load_dwordx4 v[4:7], v3, s[6:7]
	global_load_dwordx4 v[8:11], v3, s[6:7] offset:1024
	global_load_dwordx4 v[12:15], v3, s[6:7] offset:2048
	s_add_i32 s63, s62, 0x3000
	s_and_b32 s63, s63, 0x3f000
	s_or_b32 s63, s63, s66
	v_or_b32_e32 v2, s63, v231
	global_load_dwordx4 v[80:83], v2, s[6:7]
	global_load_dwordx4 v[84:87], v2, s[6:7] offset:1024
	global_load_dwordx4 v[88:91], v2, s[6:7] offset:2048
	global_load_dwordx4 v[92:95], v2, s[6:7] offset:3072
	s_add_i32 s63, s62, 0x2000
	s_and_b32 s63, s63, 0x3f000
	s_or_b32 s63, s63, s66
	v_or_b32_e32 v3, s63, v231
	global_load_dwordx4 v[96:99], v3, s[6:7]
	global_load_dwordx4 v[100:103], v3, s[6:7] offset:1024
	global_load_dwordx4 v[108:111], v3, s[6:7] offset:2048
	global_load_dwordx4 v[192:195], v3, s[6:7] offset:3072
	s_add_i32 s63, s62, 0x1000
	s_and_b32 s63, s63, 0x3f000
	s_or_b32 s63, s63, s66
	v_or_b32_e32 v2, s63, v231
	global_load_dwordx4 v[174:177], v2, s[6:7] offset:2048
	global_load_dwordx4 v[178:181], v2, s[6:7] offset:3072
	s_waitcnt vmcnt(0)
	s_branch .LBB1_14
.LBB1_13:
	s_waitcnt vmcnt(12)
	v_cvt_pk_f16_f32 v151, v120, v121
	v_cvt_pk_f16_f32 v150, v100, v101
	v_cvt_pk_f16_f32 v149, v98, v99
	v_cvt_pk_f16_f32 v148, v112, v113
	s_add_i32 s24, s57, 1
	s_cmp_lg_u32 s57, 7
	s_waitcnt vmcnt(11)
	v_mfma_f32_32x32x16_f16 v[0:15], v[144:147], v[148:151], v[0:15]
	s_cselect_b32 s59, s24, 7
	s_lshl_b32 s25, s59, 2
	s_and_b32 s25, s25, 56
	s_or_b32 s58, s25, s27
	s_lshl_b32 s25, s55, 5
	s_and_b32 s59, s59, 1
	s_waitcnt vmcnt(10)
	v_mfma_f32_32x32x16_f16 v[16:31], v[140:143], v[148:151], v[16:31]
	v_cvt_pk_f16_f32 v143, v180, v181
	v_cvt_pk_f16_f32 v142, v124, v125
	v_cvt_pk_f16_f32 v141, v122, v123
	v_cvt_pk_f16_f32 v140, v102, v103
	s_waitcnt vmcnt(9)
	s_nop 0
	v_mfma_f32_32x32x16_f16 v[0:15], v[136:139], v[140:143], v[0:15]
	s_waitcnt vmcnt(8)
	v_mfma_f32_32x32x16_f16 v[16:31], v[132:135], v[140:143], v[16:31]
	s_add_i32 s61, s35, s60
	s_and_b32 s61, s61, 0x3f000
	v_or_b32_e32 v144, s61, v248
	s_add_i32 s61, s36, s60
	s_and_b32 s61, s61, 0x3f000
	v_or_b32_e32 v160, s61, v248
	global_load_dwordx4 v[132:135], v144, s[16:17]
	global_load_dwordx4 v[136:139], v144, s[16:17] offset:1024
	global_load_dwordx4 v[140:143], v144, s[16:17] offset:2048
	s_nop 0
	global_load_dwordx4 v[144:147], v144, s[16:17] offset:3072
	s_nop 0
	global_load_dwordx4 v[148:151], v160, s[16:17]
	global_load_dwordx4 v[152:155], v160, s[16:17] offset:1024
	global_load_dwordx4 v[156:159], v160, s[16:17] offset:2048
	s_nop 0
	global_load_dwordx4 v[160:163], v160, s[16:17] offset:3072
	v_cvt_pk_f16_f32 v253, v96, v97
	v_cvt_pk_f16_f32 v252, v84, v85
	v_cvt_pk_f16_f32 v251, v82, v83
	v_cvt_pk_f16_f32 v250, v80, v81
	s_waitcnt vmcnt(15)
	s_nop 0
	v_mfma_f32_32x32x16_f16 v[0:15], v[60:63], v[250:253], v[0:15]
	s_waitcnt vmcnt(14)
	v_mfma_f32_32x32x16_f16 v[16:31], v[56:59], v[250:253], v[16:31]
	v_cvt_pk_f16_f32 v59, v94, v95
	v_cvt_pk_f16_f32 v58, v90, v91
	v_cvt_pk_f16_f32 v57, v88, v89
	v_cvt_pk_f16_f32 v56, v86, v87
	s_waitcnt vmcnt(13)
	s_nop 0
	v_mfma_f32_32x32x16_f16 v[0:15], v[52:55], v[56:59], v[0:15]
	s_waitcnt vmcnt(12)
	v_mfma_f32_32x32x16_f16 v[16:31], v[48:51], v[56:59], v[16:31]
	v_cvt_pk_f16_f32 v51, v176, v177
	v_cvt_pk_f16_f32 v50, v110, v111
	v_cvt_pk_f16_f32 v49, v108, v109
	v_cvt_pk_f16_f32 v48, v92, v93
	s_waitcnt vmcnt(11)
	s_nop 0
	v_mfma_f32_32x32x16_f16 v[0:15], v[44:47], v[48:51], v[0:15]
	s_waitcnt vmcnt(10)
	v_mfma_f32_32x32x16_f16 v[16:31], v[40:43], v[48:51], v[16:31]
	v_cvt_pk_f16_f32 v43, v206, v207
	v_cvt_pk_f16_f32 v42, v194, v195
	v_cvt_pk_f16_f32 v41, v192, v193
	v_cvt_pk_f16_f32 v40, v174, v175
	s_waitcnt vmcnt(9)
	s_nop 0
	v_mfma_f32_32x32x16_f16 v[0:15], v[36:39], v[40:43], v[0:15]
	s_waitcnt vmcnt(8)
	v_mfma_f32_32x32x16_f16 v[16:31], v[32:35], v[40:43], v[16:31]
	s_add_i32 s61, s37, s60
	s_add_i32 s60, s38, s60
	s_and_b32 s61, s61, 0x3f000
	s_and_b32 s60, s60, 0x3f000
	v_or_b32_e32 v44, s61, v248
	v_or_b32_e32 v60, s60, v248
	global_load_dwordx4 v[32:35], v44, s[16:17]
	global_load_dwordx4 v[36:39], v44, s[16:17] offset:1024
	global_load_dwordx4 v[40:43], v44, s[16:17] offset:2048
	s_nop 0
	global_load_dwordx4 v[44:47], v44, s[16:17] offset:3072
	s_nop 0
	global_load_dwordx4 v[48:51], v60, s[16:17]
	global_load_dwordx4 v[52:55], v60, s[16:17] offset:1024
	global_load_dwordx4 v[56:59], v60, s[16:17] offset:2048
	s_nop 0
	global_load_dwordx4 v[60:63], v60, s[16:17] offset:3072
	v_cvt_pk_f16_f32 v251, v74, v75
	v_cvt_pk_f16_f32 v250, v68, v69
	v_cvt_pk_f16_f32 v249, v66, v67
	v_cvt_pk_f16_f32 v248, v64, v65
	s_waitcnt vmcnt(15)
	s_nop 0
	v_mfma_f32_32x32x16_f16 v[0:15], v[132:135], v[248:251], v[0:15]
	v_cvt_pk_f16_f32 v135, v172, v173
	v_cvt_pk_f16_f32 v134, v106, v107
	v_cvt_pk_f16_f32 v133, v104, v105
	v_cvt_pk_f16_f32 v132, v72, v73
	s_waitcnt vmcnt(14)
	v_mfma_f32_32x32x16_f16 v[16:31], v[136:139], v[248:251], v[16:31]
	s_waitcnt vmcnt(13)
	v_mfma_f32_32x32x16_f16 v[0:15], v[140:143], v[132:135], v[0:15]
	s_waitcnt vmcnt(12)
	v_mfma_f32_32x32x16_f16 v[16:31], v[144:147], v[132:135], v[16:31]
	v_cvt_pk_f16_f32 v135, v202, v203
	v_cvt_pk_f16_f32 v134, v190, v191
	v_cvt_pk_f16_f32 v133, v188, v189
	v_cvt_pk_f16_f32 v132, v170, v171
	s_waitcnt vmcnt(11)
	s_nop 0
	v_mfma_f32_32x32x16_f16 v[0:15], v[148:151], v[132:135], v[0:15]
	s_waitcnt vmcnt(10)
	v_mfma_f32_32x32x16_f16 v[16:31], v[152:155], v[132:135], v[16:31]
	v_cvt_pk_f16_f32 v135, v222, v223
	v_cvt_pk_f16_f32 v134, v216, v217
	v_cvt_pk_f16_f32 v133, v214, v215
	v_cvt_pk_f16_f32 v132, v200, v201
	s_waitcnt vmcnt(9)
	s_nop 0
	v_mfma_f32_32x32x16_f16 v[0:15], v[156:159], v[132:135], v[0:15]
	s_waitcnt vmcnt(8)
	v_mfma_f32_32x32x16_f16 v[16:31], v[160:163], v[132:135], v[16:31]
	v_cvt_pk_f16_f32 v135, v168, v169
	v_cvt_pk_f16_f32 v134, v78, v79
	v_cvt_pk_f16_f32 v133, v76, v77
	v_cvt_pk_f16_f32 v132, v70, v71
	s_waitcnt vmcnt(7)
	s_nop 0
	v_mfma_f32_32x32x16_f16 v[0:15], v[32:35], v[132:135], v[0:15]
	v_cvt_pk_f16_f32 v35, v198, v199
	v_cvt_pk_f16_f32 v34, v186, v187
	v_cvt_pk_f16_f32 v33, v184, v185
	v_cvt_pk_f16_f32 v32, v126, v127
	s_waitcnt vmcnt(6)
	v_mfma_f32_32x32x16_f16 v[16:31], v[36:39], v[132:135], v[16:31]
	s_waitcnt vmcnt(5)
	v_mfma_f32_32x32x16_f16 v[0:15], v[40:43], v[32:35], v[0:15]
	s_waitcnt vmcnt(4)
	v_mfma_f32_32x32x16_f16 v[16:31], v[44:47], v[32:35], v[16:31]
	v_cvt_pk_f16_f32 v35, v220, v221
	v_cvt_pk_f16_f32 v34, v212, v213
	v_cvt_pk_f16_f32 v33, v210, v211
	v_cvt_pk_f16_f32 v32, v196, v197
	s_waitcnt vmcnt(3)
	s_nop 0
	v_mfma_f32_32x32x16_f16 v[0:15], v[48:51], v[32:35], v[0:15]
	s_waitcnt vmcnt(2)
	v_mfma_f32_32x32x16_f16 v[16:31], v[52:55], v[32:35], v[16:31]
	v_cvt_pk_f16_f32 v35, v228, v229
	v_cvt_pk_f16_f32 v34, v226, v227
	v_cvt_pk_f16_f32 v33, v224, v225
	v_cvt_pk_f16_f32 v32, v218, v219
	s_waitcnt vmcnt(1)
	s_nop 0
	v_mfma_f32_32x32x16_f16 v[0:15], v[56:59], v[32:35], v[0:15]
	s_waitcnt vmcnt(0)
	v_mfma_f32_32x32x16_f16 v[16:31], v[60:63], v[32:35], v[16:31]
	s_cmp_lt_u32 s31, 0x200
	s_cbranch_scc0 .Lka_late
	s_or_b32 s62, s39, s59
	s_lshl_b32 s62, s62, 12
	s_lshl_b32 s66, s58, 18
	s_and_b32 s63, s62, 0x3f000
	s_or_b32 s63, s63, s66
	v_or_b32_e32 v252, s63, v231
	global_load_dwordx4 v[48:51], v252, s[6:7]
	global_load_dwordx4 v[52:55], v252, s[6:7] offset:1024
	global_load_dwordx4 v[56:59], v252, s[6:7] offset:2048
	global_load_dwordx4 v[60:63], v252, s[6:7] offset:3072
	s_add_i32 s63, s62, 0x4000
	s_and_b32 s63, s63, 0x3f000
	s_or_b32 s63, s63, s66
	v_or_b32_e32 v253, s63, v231
	global_load_dwordx4 v[40:43], v253, s[6:7] offset:2048
	global_load_dwordx4 v[44:47], v253, s[6:7] offset:3072
	s_add_i32 s63, s62, 0x6000
	s_and_b32 s63, s63, 0x3f000
	s_or_b32 s63, s63, s66
	v_or_b32_e32 v252, s63, v231
	global_load_dwordx4 v[148:151], v252, s[6:7] offset:3072
	s_add_i32 s63, s62, 0x7000
	s_and_b32 s63, s63, 0x3f000
	s_or_b32 s63, s63, s66
	v_or_b32_e32 v253, s63, v231
	global_load_dwordx4 v[132:135], v253, s[6:7]
	global_load_dwordx4 v[136:139], v253, s[6:7] offset:1024
	global_load_dwordx4 v[140:143], v253, s[6:7] offset:2048
	global_load_dwordx4 v[144:147], v253, s[6:7] offset:3072
	s_add_i32 s63, s62, 0x1000
	s_and_b32 s63, s63, 0x3f000
	s_or_b32 s63, s63, s66
	v_or_b32_e32 v252, s63, v231
	global_load_dwordx4 v[152:155], v252, s[6:7]
	global_load_dwordx4 v[156:159], v252, s[6:7] offset:1024
	s_cmp_eq_u32 s12, 0
	s_cbranch_scc1 .Lduty_done
	v_or_b32_e32 v252, s73, v239
	v_lshl_or_b32 v252, v252, 13, v240
	v_add_lshl_u32 v253, v241, s72, 7
	v_add_u32_e32 v253, 0x300, v253
	v_and_or_b32 v252, v253, s54, v252
	ds_read_b128 v[32:35], v246
	ds_read_b128 v[36:39], v246 offset:1088
	s_waitcnt lgkmcnt(1)
	global_store_dwordx4 v252, v[32:35], s[10:11] nt
	s_nop 0
	ds_read_b128 v[32:35], v246 offset:2176
	v_or_b32_e32 v253, 0x8000, v252
	s_waitcnt lgkmcnt(1)
	global_store_dwordx4 v253, v[36:39], s[10:11] nt
	s_nop 0
	ds_read_b128 v[36:39], v246 offset:3264
	v_or_b32_e32 v253, 0x10000, v252
	s_waitcnt lgkmcnt(1)
	global_store_dwordx4 v253, v[32:35], s[10:11] nt
	s_nop 0
	ds_read_b128 v[32:35], v246 offset:4352
	v_or_b32_e32 v253, 0x18000, v252
	s_waitcnt lgkmcnt(1)
	global_store_dwordx4 v253, v[36:39], s[10:11] nt
	s_nop 0
	ds_read_b128 v[36:39], v246 offset:5440
	v_or_b32_e32 v253, 0x20000, v252
	s_waitcnt lgkmcnt(1)
	global_store_dwordx4 v253, v[32:35], s[10:11] nt
	s_nop 0
	ds_read_b128 v[32:35], v246 offset:6528
	v_or_b32_e32 v253, 0x28000, v252
	s_waitcnt lgkmcnt(1)
	global_store_dwordx4 v253, v[36:39], s[10:11] nt
	s_nop 0
	ds_read_b128 v[36:39], v246 offset:7616
	v_or_b32_e32 v253, 0x30000, v252
	s_waitcnt lgkmcnt(1)
	global_store_dwordx4 v253, v[32:35], s[10:11] nt
	v_or_b32_e32 v253, 0x38000, v252
	s_waitcnt lgkmcnt(0)
	global_store_dwordx4 v253, v[36:39], s[10:11] nt
	v_mov_b32_e32 v252, s74
	s_movk_i32 s76, 0x1000
.Lduty_poll:
	ds_read_b32 v253, v252
	s_waitcnt lgkmcnt(0)
	v_readfirstlane_b32 s75, v253
	s_cmp_eq_u32 s75, s12
	s_cbranch_scc1 .Lduty_go
	s_sleep 2
	s_sub_u32 s76, s76, 1
	s_cmp_eq_u32 s76, 0
	s_cbranch_scc0 .Lduty_poll
.Lduty_go:
	v_or_b32_e32 v252, s73, v239
	v_lshl_or_b32 v252, v252, 13, v240
	v_add_u32_e32 v253, 32, v241
	v_add_lshl_u32 v253, v253, s72, 7
	v_add_u32_e32 v253, 0x300, v253
	v_and_or_b32 v252, v253, s54, v252
	ds_read_b128 v[32:35], v246 offset:34816
	ds_read_b128 v[36:39], v246 offset:35904
	s_waitcnt lgkmcnt(1)
	global_store_dwordx4 v252, v[32:35], s[10:11] nt
	s_nop 0
	ds_read_b128 v[32:35], v246 offset:36992
	v_or_b32_e32 v253, 0x8000, v252
	s_waitcnt lgkmcnt(1)
	global_store_dwordx4 v253, v[36:39], s[10:11] nt
	s_nop 0
	ds_read_b128 v[36:39], v246 offset:38080
	v_or_b32_e32 v253, 0x10000, v252
	s_waitcnt lgkmcnt(1)
	global_store_dwordx4 v253, v[32:35], s[10:11] nt
	s_nop 0
	ds_read_b128 v[32:35], v246 offset:39168
	v_or_b32_e32 v253, 0x18000, v252
	s_waitcnt lgkmcnt(1)
	global_store_dwordx4 v253, v[36:39], s[10:11] nt
	s_nop 0
	ds_read_b128 v[36:39], v246 offset:40256
	v_or_b32_e32 v253, 0x20000, v252
	s_waitcnt lgkmcnt(1)
	global_store_dwordx4 v253, v[32:35], s[10:11] nt
	s_nop 0
	ds_read_b128 v[32:35], v246 offset:41344
	v_or_b32_e32 v253, 0x28000, v252
	s_waitcnt lgkmcnt(1)
	global_store_dwordx4 v253, v[36:39], s[10:11] nt
	s_nop 0
	ds_read_b128 v[36:39], v246 offset:42432
	v_or_b32_e32 v253, 0x30000, v252
	s_waitcnt lgkmcnt(1)
	global_store_dwordx4 v253, v[32:35], s[10:11] nt
	v_or_b32_e32 v253, 0x38000, v252
	s_waitcnt lgkmcnt(0)
	global_store_dwordx4 v253, v[36:39], s[10:11] nt
.Lduty_done:
.Lka_late:
	s_nop 9
	v_mul_f32_e64 v0, s18, v0
	v_mul_f32_e64 v1, s19, v1
	v_mul_f32_e64 v2, s18, v2
	v_mul_f32_e64 v3, s19, v3
	v_pk_mul_f32 v[16:17], s[18:19], v[16:17]
	v_pk_mul_f32 v[18:19], s[18:19], v[18:19]
	ds_write_b128 v164, v[0:3]
	ds_write_b128 v164, v[16:19] offset:128
	v_pk_mul_f32 v[0:1], s[18:19], v[4:5]
	v_pk_mul_f32 v[2:3], s[18:19], v[6:7]
	v_pk_mul_f32 v[4:5], s[18:19], v[20:21]
	v_pk_mul_f32 v[6:7], s[18:19], v[22:23]
	ds_write_b128 v164, v[0:3] offset:32
	ds_write_b128 v164, v[4:7] offset:160
	v_pk_mul_f32 v[0:1], s[18:19], v[8:9]
	v_pk_mul_f32 v[2:3], s[18:19], v[10:11]
	v_pk_mul_f32 v[4:5], s[18:19], v[24:25]
	v_pk_mul_f32 v[6:7], s[18:19], v[26:27]
	ds_write_b128 v164, v[0:3] offset:64
	ds_write_b128 v164, v[4:7] offset:192
	v_pk_mul_f32 v[0:1], s[18:19], v[12:13]
	v_pk_mul_f32 v[2:3], s[18:19], v[14:15]
	v_pk_mul_f32 v[4:5], s[18:19], v[28:29]
	v_pk_mul_f32 v[6:7], s[18:19], v[30:31]
	ds_write_b128 v164, v[0:3] offset:96
	ds_write_b128 v164, v[4:7] offset:224
	s_waitcnt lgkmcnt(0)
	s_barrier
	s_cmp_lt_u32 s31, 0x200
	s_cbranch_scc1 .Lka_done
	s_or_b32 s62, s39, s59
	s_lshl_b32 s62, s62, 12
	s_lshl_b32 s66, s58, 18
	s_and_b32 s63, s62, 0x3f000
	s_or_b32 s63, s63, s66
	v_or_b32_e32 v252, s63, v231
	global_load_dwordx4 v[48:51], v252, s[6:7]
	global_load_dwordx4 v[52:55], v252, s[6:7] offset:1024
	global_load_dwordx4 v[56:59], v252, s[6:7] offset:2048
	global_load_dwordx4 v[60:63], v252, s[6:7] offset:3072
	s_add_i32 s63, s62, 0x4000
	s_and_b32 s63, s63, 0x3f000
	s_or_b32 s63, s63, s66
	v_or_b32_e32 v253, s63, v231
	global_load_dwordx4 v[40:43], v253, s[6:7] offset:2048
	global_load_dwordx4 v[44:47], v253, s[6:7] offset:3072
	s_add_i32 s63, s62, 0x6000
	s_and_b32 s63, s63, 0x3f000
	s_or_b32 s63, s63, s66
	v_or_b32_e32 v252, s63, v231
	global_load_dwordx4 v[148:151], v252, s[6:7] offset:3072
	s_add_i32 s63, s62, 0x7000
	s_and_b32 s63, s63, 0x3f000
	s_or_b32 s63, s63, s66
	v_or_b32_e32 v253, s63, v231
	global_load_dwordx4 v[132:135], v253, s[6:7]
	global_load_dwordx4 v[136:139], v253, s[6:7] offset:1024
	global_load_dwordx4 v[140:143], v253, s[6:7] offset:2048
	global_load_dwordx4 v[144:147], v253, s[6:7] offset:3072
	s_add_i32 s63, s62, 0x1000
	s_and_b32 s63, s63, 0x3f000
	s_or_b32 s63, s63, s66
	v_or_b32_e32 v252, s63, v231
	global_load_dwordx4 v[152:155], v252, s[6:7]
	global_load_dwordx4 v[156:159], v252, s[6:7] offset:1024
.Lka_done:
	ds_read2_b32 v[0:1], v235 offset1:32
	ds_read2_b32 v[2:3], v235 offset0:64 offset1:96
	ds_read2_b32 v[4:5], v235 offset0:128 offset1:160
	ds_read2_b32 v[6:7], v235 offset0:192 offset1:224
	ds_read2_b32 v[10:11], v236 offset0:128 offset1:160
	ds_read2_b32 v[16:17], v165 offset1:32
	ds_write_b128 v232, v[128:131]
	s_waitcnt lgkmcnt(6)
	v_max_f32_e32 v8, v1, v1
	v_max_f32_e32 v9, v0, v0
	v_max_f32_e32 v8, v9, v8
	s_waitcnt lgkmcnt(5)
	v_max3_f32 v8, v8, v2, v3
	s_waitcnt lgkmcnt(4)
	v_max3_f32 v8, v8, v4, v5
	s_waitcnt lgkmcnt(3)
	v_max3_f32 v14, v8, v6, v7
	ds_read2_b32 v[8:9], v236 offset1:32
	v_sub_f32_e32 v0, v0, v14
	v_sub_f32_e32 v1, v1, v14
	v_exp_f32_e32 v0, v0
	v_exp_f32_e32 v1, v1
	v_sub_f32_e32 v4, v4, v14
	v_sub_f32_e32 v5, v5, v14
	v_exp_f32_e32 v4, v4
	v_exp_f32_e32 v5, v5
	s_waitcnt lgkmcnt(0)
	v_pk_mul_f32 v[0:1], v[8:9], v[0:1]
	ds_read2_b32 v[8:9], v236 offset0:64 offset1:96
	v_sub_f32_e32 v2, v2, v14
	v_sub_f32_e32 v3, v3, v14
	v_exp_f32_e32 v2, v2
	v_exp_f32_e32 v3, v3
	ds_read2_b32 v[12:13], v236 offset0:192 offset1:224
	v_sub_f32_e32 v6, v6, v14
	v_sub_f32_e32 v7, v7, v14
	v_pk_mul_f32 v[18:19], v[10:11], v[4:5]
	v_sub_f32_e32 v4, v247, v14
	ds_read2_b32 v[22:23], v165 offset0:64 offset1:96
	ds_read2_b32 v[24:25], v165 offset0:128 offset1:160
	ds_read2_b32 v[26:27], v165 offset0:192 offset1:224
	v_exp_f32_e32 v6, v6
	v_exp_f32_e32 v7, v7
	v_exp_f32_e32 v34, v4
	v_max_f32_e32 v4, v17, v17
	v_max_f32_e32 v5, v16, v16
	v_add_f32_e32 v0, 0, v0
	s_waitcnt lgkmcnt(4)
	v_pk_mul_f32 v[2:3], v[8:9], v[2:3]
	v_max_f32_e32 v4, v5, v4
	v_add_f32_e32 v0, v0, v1
	s_waitcnt lgkmcnt(2)
	v_max3_f32 v4, v4, v22, v23
	v_add_f32_e32 v0, v0, v2
	s_waitcnt lgkmcnt(1)
	v_max3_f32 v4, v4, v24, v25
	v_add_f32_e32 v0, v0, v3
	v_pk_mul_f32 v[20:21], v[12:13], v[6:7]
	s_waitcnt lgkmcnt(0)
	v_max3_f32 v35, v4, v26, v27
	v_add_f32_e32 v18, v0, v18
	ds_read_b128 v[0:3], v245
	ds_read_b128 v[4:7], v237
	v_sub_f32_e32 v8, v16, v35
	v_exp_f32_e32 v16, v8
	ds_read2_b32 v[28:29], v242 offset1:32
	ds_read_b128 v[8:11], v245 offset:34816
	ds_read_b128 v[12:15], v245 offset:60928
	s_min_u32 s57, s57, 5
	s_waitcnt lgkmcnt(3)
	v_pk_add_f32 v[0:1], v[0:1], v[4:5]
	v_pk_add_f32 v[2:3], v[2:3], v[6:7]
	v_pk_fma_f32 v[30:31], v[16:17], v[0:1], 0 op_sel_hi:[0,1,0]
	v_sub_f32_e32 v0, v17, v35
	v_pk_fma_f32 v[32:33], v[16:17], v[2:3], 0 op_sel_hi:[0,1,0]
	v_exp_f32_e32 v17, v0
	v_add_f32_e32 v0, v18, v19
	v_add_f32_e32 v0, v0, v20
	v_add_f32_e32 v36, v0, v21
	ds_read_b128 v[0:3], v245 offset:8704
	ds_read_b128 v[4:7], v245 offset:17408
	s_waitcnt lgkmcnt(4)
	v_pk_mul_f32 v[18:19], v[28:29], v[16:17]
	v_sub_f32_e32 v16, v22, v35
	v_exp_f32_e32 v16, v16
	v_add_f32_e32 v20, 0, v18
	v_mov_b32_e32 v18, v17
	s_waitcnt lgkmcnt(1)
	v_pk_fma_f32 v[0:1], v[18:19], v[0:1], v[30:31] op_sel_hi:[0,1,1]
	v_pk_fma_f32 v[2:3], v[18:19], v[2:3], v[32:33] op_sel_hi:[0,1,1]
	s_waitcnt lgkmcnt(0)
	v_pk_fma_f32 v[4:5], v[16:17], v[4:5], v[0:1] op_sel_hi:[0,1,1]
	v_sub_f32_e32 v0, v23, v35
	v_pk_fma_f32 v[6:7], v[16:17], v[6:7], v[2:3] op_sel_hi:[0,1,1]
	v_exp_f32_e32 v17, v0
	v_add_f32_e32 v21, v20, v19
	ds_read_b128 v[0:3], v245 offset:26112
	ds_read2_b32 v[18:19], v242 offset0:64 offset1:96
	v_sub_f32_e32 v22, v24, v35
	v_exp_f32_e32 v22, v22
	v_mov_b32_e32 v20, v17
	s_waitcnt lgkmcnt(1)
	v_pk_fma_f32 v[0:1], v[20:21], v[0:1], v[4:5] op_sel_hi:[0,1,1]
	v_pk_fma_f32 v[2:3], v[20:21], v[2:3], v[6:7] op_sel_hi:[0,1,1]
	ds_read2_b32 v[4:5], v242 offset0:128 offset1:160
	v_pk_fma_f32 v[8:9], v[22:23], v[8:9], v[0:1] op_sel_hi:[0,1,1]
	v_sub_f32_e32 v0, v25, v35
	v_pk_fma_f32 v[10:11], v[22:23], v[10:11], v[2:3] op_sel_hi:[0,1,1]
	v_exp_f32_e32 v23, v0
	s_waitcnt lgkmcnt(1)
	v_pk_mul_f32 v[0:1], v[18:19], v[16:17]
	s_lshl_b32 s58, s58, 18
	v_add_f32_e32 v0, v21, v0
	v_add_f32_e32 v2, v0, v1
	s_waitcnt lgkmcnt(0)
	v_pk_mul_f32 v[0:1], v[4:5], v[22:23]
	v_sub_f32_e32 v4, v26, v35
	v_add_f32_e32 v0, v2, v0
	v_add_f32_e32 v17, v0, v1
	ds_read_b128 v[0:3], v245 offset:43520
	v_exp_f32_e32 v18, v4
	ds_read2_b32 v[20:21], v242 offset0:192 offset1:224
	v_sub_f32_e32 v4, v27, v35
	v_exp_f32_e32 v19, v4
	ds_read_b128 v[4:7], v245 offset:52224
	v_mov_b32_e32 v16, v23
	s_waitcnt lgkmcnt(2)
	v_pk_fma_f32 v[0:1], v[16:17], v[0:1], v[8:9] op_sel_hi:[0,1,1]
	s_waitcnt lgkmcnt(1)
	v_pk_mul_f32 v[8:9], v[20:21], v[18:19]
	v_pk_fma_f32 v[2:3], v[16:17], v[2:3], v[10:11] op_sel_hi:[0,1,1]
	v_add_f32_e32 v8, v17, v8
	v_add_f32_e32 v8, v8, v9
	s_waitcnt lgkmcnt(0)
	v_pk_fma_f32 v[0:1], v[18:19], v[4:5], v[0:1] op_sel_hi:[0,1,1]
	v_div_scale_f32 v5, s[60:61], v8, v8, 1.0
	v_pk_fma_f32 v[2:3], v[18:19], v[6:7], v[2:3] op_sel_hi:[0,1,1]
	v_rcp_f32_e32 v6, v5
	v_mov_b32_e32 v4, v19
	v_pk_fma_f32 v[2:3], v[4:5], v[14:15], v[2:3] op_sel_hi:[0,1,1]
	v_pk_fma_f32 v[0:1], v[4:5], v[12:13], v[0:1] op_sel_hi:[0,1,1]
	v_fma_f32 v4, -v5, v6, 1.0
	v_fmac_f32_e32 v6, v4, v6
	v_div_scale_f32 v4, vcc, 1.0, v8, 1.0
	v_mul_f32_e32 v7, v4, v6
	v_fma_f32 v9, -v5, v7, v4
	v_fmac_f32_e32 v7, v9, v6
	v_fma_f32 v4, -v5, v7, v4
	v_div_fmas_f32 v4, v4, v6, v7
	s_lshl_b32 s60, s56, 19
	s_lshl_b32 s61, s55, 13
	v_div_fixup_f32 v4, v4, v8, 1.0
	s_add_i32 s60, s60, s61
	v_pk_mul_f32 v[2:3], v[2:3], v[4:5] op_sel_hi:[1,0]
	v_pk_mul_f32 v[0:1], v[0:1], v[4:5] op_sel_hi:[1,0]
	v_or_b32_e32 v4, s60, v230
	s_lshl_b32 s60, s57, 2
	s_add_i32 s60, s60, 8
	s_and_b32 s60, s60, 56
	s_and_b32 s57, s57, 1
	s_or_b32 s60, s60, s27
	s_or_b32 s57, s57, s28
	s_lshl_b32 s60, s60, 19
	s_lshl_b32 s57, s57, 13
	s_add_i32 s60, s60, s57
	s_or_b32 s62, s39, s59
	s_lshl_b32 s62, s62, 12
	global_store_dwordx4 v4, v[0:3], s[8:9] nt
	v_mov_b32_e32 v252, v34
	v_mov_b32_e32 v253, v36
	v_or_b32_e32 v0, s60, v230
	s_barrier
	global_load_dwordx4 v[128:131], v0, s[4:5]
	s_add_i32 s63, s62, 0x4000
	s_and_b32 s63, s63, 0x3f000
	s_or_b32 s63, s63, s58
	v_or_b32_e32 v2, s63, v231
	global_load_dwordx4 v[32:35], v2, s[6:7]
	global_load_dwordx4 v[36:39], v2, s[6:7] offset:1024
	s_add_i32 s63, s62, 0x5000
	s_and_b32 s63, s63, 0x3f000
	s_or_b32 s63, s63, s58
	v_or_b32_e32 v3, s63, v231
	global_load_dwordx4 v[16:19], v3, s[6:7]
	global_load_dwordx4 v[20:23], v3, s[6:7] offset:1024
	global_load_dwordx4 v[24:27], v3, s[6:7] offset:2048
	global_load_dwordx4 v[28:31], v3, s[6:7] offset:3072
	s_add_i32 s63, s62, 0x6000
	s_and_b32 s63, s63, 0x3f000
	s_or_b32 s63, s63, s58
	v_or_b32_e32 v2, s63, v231
	global_load_dwordx4 v[4:7], v2, s[6:7]
	global_load_dwordx4 v[8:11], v2, s[6:7] offset:1024
	global_load_dwordx4 v[12:15], v2, s[6:7] offset:2048
	v_div_scale_f32 v1, s[64:65], v253, v253, v252
	v_rcp_f32_e32 v2, v1
	s_nop 0
	v_fma_f32 v0, -v1, v2, 1.0
	v_fmac_f32_e32 v2, v0, v2
	v_div_scale_f32 v0, vcc, v252, v253, v252
	v_mul_f32_e32 v3, v0, v2
	v_fma_f32 v248, -v1, v3, v0
	v_fmac_f32_e32 v3, v248, v2
	v_fma_f32 v0, -v1, v3, v0
	v_div_fmas_f32 v0, v0, v2, v3
	v_div_fixup_f32 v1, v0, v253, v252
	v_mul_f32_e32 v0, s18, v1
	v_mov_b32_e32 v2, s26
	v_mov_b32_e32 v3, s23
	v_cmp_eq_u32_e64 s[64:65], 0, v233
	v_cmp_eq_u32_e64 s[66:67], 1, v233
	v_cmp_eq_u32_e64 s[68:69], 2, v233
	v_cmp_eq_u32_e64 s[70:71], 3, v233
	v_cndmask_b32_e64 v248, v2, v3, s[64:65]
	v_cndmask_b32_e64 v249, v2, v3, s[66:67]
	v_cndmask_b32_e64 v250, v2, v3, s[68:69]
	v_cndmask_b32_e64 v251, v2, v3, s[70:71]
	v_mul_f32_e32 v248, v1, v248
	v_mul_f32_e32 v249, v1, v249
	v_mul_f32_e32 v250, v1, v250
	v_mul_f32_e32 v251, v1, v251
	v_cndmask_b32_e64 v248, v0, v248, s[2:3]
	v_cndmask_b32_e64 v249, v0, v249, s[2:3]
	v_cndmask_b32_e64 v250, v0, v250, s[2:3]
	v_cndmask_b32_e64 v251, v0, v251, s[2:3]
	v_mul_f32_e32 v248, v248, v208
	v_mul_f32_e32 v249, v249, v209
	v_mul_f32_e32 v250, v250, v204
	v_mul_f32_e32 v251, v251, v205
	ds_write_b128 v238, v[248:251]
	v_cmp_eq_u32_e64 s[64:65], 4, v233
	v_cmp_eq_u32_e64 s[66:67], 5, v233
	v_cmp_eq_u32_e64 s[68:69], 6, v233
	v_cmp_eq_u32_e64 s[70:71], 7, v233
	v_cndmask_b32_e64 v248, v2, v3, s[64:65]
	v_cndmask_b32_e64 v249, v2, v3, s[66:67]
	v_cndmask_b32_e64 v250, v2, v3, s[68:69]
	v_cndmask_b32_e64 v251, v2, v3, s[70:71]
	v_mul_f32_e32 v248, v1, v248
	v_mul_f32_e32 v249, v1, v249
	v_mul_f32_e32 v250, v1, v250
	v_mul_f32_e32 v251, v1, v251
	v_cndmask_b32_e64 v248, v0, v248, s[2:3]
	v_cndmask_b32_e64 v249, v0, v249, s[2:3]
	v_cndmask_b32_e64 v250, v0, v250, s[2:3]
	v_cndmask_b32_e64 v251, v0, v251, s[2:3]
	v_mul_f32_e32 v248, v248, v182
	v_mul_f32_e32 v249, v249, v183
	v_mul_f32_e32 v250, v250, v178
	v_mul_f32_e32 v251, v251, v179
	ds_write_b128 v238, v[248:251] offset:32
	v_cmp_eq_u32_e64 s[64:65], 8, v233
	v_cmp_eq_u32_e64 s[66:67], 9, v233
	v_cmp_eq_u32_e64 s[68:69], 10, v233
	v_cmp_eq_u32_e64 s[70:71], 11, v233
	v_cndmask_b32_e64 v248, v2, v3, s[64:65]
	v_cndmask_b32_e64 v249, v2, v3, s[66:67]
	v_cndmask_b32_e64 v250, v2, v3, s[68:69]
	v_cndmask_b32_e64 v251, v2, v3, s[70:71]
	v_mul_f32_e32 v248, v1, v248
	v_mul_f32_e32 v249, v1, v249
	v_mul_f32_e32 v250, v1, v250
	v_mul_f32_e32 v251, v1, v251
	v_cndmask_b32_e64 v248, v0, v248, s[2:3]
	v_cndmask_b32_e64 v249, v0, v249, s[2:3]
	v_cndmask_b32_e64 v250, v0, v250, s[2:3]
	v_cndmask_b32_e64 v251, v0, v251, s[2:3]
	v_mul_f32_e32 v248, v248, v166
	v_mul_f32_e32 v249, v249, v167
	v_mul_f32_e32 v250, v250, v118
	v_mul_f32_e32 v251, v251, v119
	ds_write_b128 v238, v[248:251] offset:64
	v_cmp_eq_u32_e64 s[64:65], 12, v233
	v_cmp_eq_u32_e64 s[66:67], 13, v233
	v_cmp_eq_u32_e64 s[68:69], 14, v233
	v_cmp_eq_u32_e64 s[70:71], 15, v233
	v_cndmask_b32_e64 v248, v2, v3, s[64:65]
	v_cndmask_b32_e64 v249, v2, v3, s[66:67]
	v_cndmask_b32_e64 v250, v2, v3, s[68:69]
	v_cndmask_b32_e64 v251, v2, v3, s[70:71]
	v_mul_f32_e32 v248, v1, v248
	v_mul_f32_e32 v249, v1, v249
	v_mul_f32_e32 v250, v1, v250
	v_mul_f32_e32 v251, v1, v251
	v_cndmask_b32_e64 v248, v0, v248, s[2:3]
	v_cndmask_b32_e64 v249, v0, v249, s[2:3]
	v_cndmask_b32_e64 v250, v0, v250, s[2:3]
	v_cndmask_b32_e64 v251, v0, v251, s[2:3]
	v_mul_f32_e32 v248, v248, v116
	v_mul_f32_e32 v249, v249, v117
	v_mul_f32_e32 v250, v250, v114
	v_mul_f32_e32 v251, v251, v115
	ds_write_b128 v238, v[248:251] offset:96
	v_pk_mul_f32 v[248:249], v[0:1], v[112:113] op_sel_hi:[0,1]
	v_pk_mul_f32 v[250:251], v[0:1], v[98:99] op_sel_hi:[0,1]
	ds_write_b128 v238, v[248:251] offset:128
	v_pk_mul_f32 v[248:249], v[0:1], v[100:101] op_sel_hi:[0,1]
	v_pk_mul_f32 v[250:251], v[0:1], v[120:121] op_sel_hi:[0,1]
	ds_write_b128 v238, v[248:251] offset:160
	v_pk_mul_f32 v[248:249], v[0:1], v[102:103] op_sel_hi:[0,1]
	v_pk_mul_f32 v[250:251], v[0:1], v[122:123] op_sel_hi:[0,1]
	ds_write_b128 v238, v[248:251] offset:192
	v_pk_mul_f32 v[248:249], v[0:1], v[124:125] op_sel_hi:[0,1]
	v_pk_mul_f32 v[250:251], v[0:1], v[180:181] op_sel_hi:[0,1]
	ds_write_b128 v238, v[248:251] offset:224
	s_lshl_b32 s56, s56, 11
	s_add_i32 s56, s56, s25
	v_or_b32_e32 v252, s56, v239
	v_add_lshl_u32 v253, v241, s55, 7
	v_lshl_or_b32 v1, v252, 13, v240
	v_and_or_b32 v2, v253, s54, v1
	ds_read_b128 v[248:251], v246
	ds_read_b128 v[160:163], v246 offset:1088
	s_waitcnt lgkmcnt(1)
	global_store_dwordx4 v2, v[248:251], s[10:11] nt
	s_nop 0
	ds_read_b128 v[248:251], v246 offset:2176
	v_or_b32_e32 v3, 0x8000, v2
	s_waitcnt lgkmcnt(1)
	global_store_dwordx4 v3, v[160:163], s[10:11] nt
	s_nop 0
	ds_read_b128 v[160:163], v246 offset:3264
	v_or_b32_e32 v252, 0x10000, v2
	s_waitcnt lgkmcnt(1)
	global_store_dwordx4 v252, v[248:251], s[10:11] nt
	s_nop 0
	ds_read_b128 v[248:251], v246 offset:4352
	v_or_b32_e32 v3, 0x18000, v2
	s_waitcnt lgkmcnt(1)
	global_store_dwordx4 v3, v[160:163], s[10:11] nt
	s_nop 0
	ds_read_b128 v[160:163], v246 offset:5440
	v_or_b32_e32 v252, 0x20000, v2
	s_waitcnt lgkmcnt(1)
	global_store_dwordx4 v252, v[248:251], s[10:11] nt
	s_nop 0
	ds_read_b128 v[248:251], v246 offset:6528
	v_or_b32_e32 v3, 0x28000, v2
	s_waitcnt lgkmcnt(1)
	global_store_dwordx4 v3, v[160:163], s[10:11] nt
	s_nop 0
	ds_read_b128 v[160:163], v246 offset:7616
	v_or_b32_e32 v252, 0x30000, v2
	s_waitcnt lgkmcnt(1)
	global_store_dwordx4 v252, v[248:251], s[10:11] nt
	v_or_b32_e32 v3, 0x38000, v2
	s_waitcnt lgkmcnt(0)
	global_store_dwordx4 v3, v[160:163], s[10:11] nt
	v_pk_mul_f32 v[248:249], v[0:1], v[80:81] op_sel_hi:[0,1]
	v_pk_mul_f32 v[250:251], v[0:1], v[82:83] op_sel_hi:[0,1]
	ds_write_b128 v238, v[248:251]
	v_pk_mul_f32 v[248:249], v[0:1], v[84:85] op_sel_hi:[0,1]
	v_pk_mul_f32 v[250:251], v[0:1], v[96:97] op_sel_hi:[0,1]
	ds_write_b128 v238, v[248:251] offset:32
	v_pk_mul_f32 v[248:249], v[0:1], v[86:87] op_sel_hi:[0,1]
	v_pk_mul_f32 v[250:251], v[0:1], v[88:89] op_sel_hi:[0,1]
	ds_write_b128 v238, v[248:251] offset:64
	v_pk_mul_f32 v[248:249], v[0:1], v[90:91] op_sel_hi:[0,1]
	v_pk_mul_f32 v[250:251], v[0:1], v[94:95] op_sel_hi:[0,1]
	ds_write_b128 v238, v[248:251] offset:96
	v_pk_mul_f32 v[248:249], v[0:1], v[92:93] op_sel_hi:[0,1]
	v_pk_mul_f32 v[250:251], v[0:1], v[108:109] op_sel_hi:[0,1]
	ds_write_b128 v238, v[248:251] offset:128
	v_pk_mul_f32 v[248:249], v[0:1], v[110:111] op_sel_hi:[0,1]
	v_pk_mul_f32 v[250:251], v[0:1], v[176:177] op_sel_hi:[0,1]
	ds_write_b128 v238, v[248:251] offset:160
	v_pk_mul_f32 v[248:249], v[0:1], v[174:175] op_sel_hi:[0,1]
	v_pk_mul_f32 v[250:251], v[0:1], v[192:193] op_sel_hi:[0,1]
	ds_write_b128 v238, v[248:251] offset:192
	v_pk_mul_f32 v[248:249], v[0:1], v[194:195] op_sel_hi:[0,1]
	v_pk_mul_f32 v[250:251], v[0:1], v[206:207] op_sel_hi:[0,1]
	ds_write_b128 v238, v[248:251] offset:224
	v_add_u32_e32 v252, 0x100, v253
	v_and_or_b32 v2, v252, s54, v1
	ds_read_b128 v[248:251], v246
	ds_read_b128 v[160:163], v246 offset:1088
	s_waitcnt lgkmcnt(1)
	global_store_dwordx4 v2, v[248:251], s[10:11] nt
	s_nop 0
	ds_read_b128 v[248:251], v246 offset:2176
	v_or_b32_e32 v3, 0x8000, v2
	s_waitcnt lgkmcnt(1)
	global_store_dwordx4 v3, v[160:163], s[10:11] nt
	s_nop 0
	ds_read_b128 v[160:163], v246 offset:3264
	v_or_b32_e32 v252, 0x10000, v2
	s_waitcnt lgkmcnt(1)
	global_store_dwordx4 v252, v[248:251], s[10:11] nt
	s_nop 0
	ds_read_b128 v[248:251], v246 offset:4352
	v_or_b32_e32 v3, 0x18000, v2
	s_waitcnt lgkmcnt(1)
	global_store_dwordx4 v3, v[160:163], s[10:11] nt
	s_nop 0
	ds_read_b128 v[160:163], v246 offset:5440
	v_or_b32_e32 v252, 0x20000, v2
	s_waitcnt lgkmcnt(1)
	global_store_dwordx4 v252, v[248:251], s[10:11] nt
	s_nop 0
	ds_read_b128 v[248:251], v246 offset:6528
	v_or_b32_e32 v3, 0x28000, v2
	s_waitcnt lgkmcnt(1)
	global_store_dwordx4 v3, v[160:163], s[10:11] nt
	s_nop 0
	ds_read_b128 v[160:163], v246 offset:7616
	v_or_b32_e32 v252, 0x30000, v2
	s_waitcnt lgkmcnt(1)
	global_store_dwordx4 v252, v[248:251], s[10:11] nt
	v_or_b32_e32 v3, 0x38000, v2
	s_waitcnt lgkmcnt(0)
	global_store_dwordx4 v3, v[160:163], s[10:11] nt
	s_add_i32 s63, s62, 0x3000
	s_and_b32 s63, s63, 0x3f000
	s_or_b32 s63, s63, s58
	v_or_b32_e32 v2, s63, v231
	global_load_dwordx4 v[80:83], v2, s[6:7]
	global_load_dwordx4 v[84:87], v2, s[6:7] offset:1024
	global_load_dwordx4 v[88:91], v2, s[6:7] offset:2048
	global_load_dwordx4 v[92:95], v2, s[6:7] offset:3072
	s_add_i32 s63, s62, 0x2000
	s_and_b32 s63, s63, 0x3f000
	s_or_b32 s63, s63, s58
	v_or_b32_e32 v3, s63, v231
	global_load_dwordx4 v[96:99], v3, s[6:7]
	global_load_dwordx4 v[100:103], v3, s[6:7] offset:1024
	global_load_dwordx4 v[108:111], v3, s[6:7] offset:2048
	global_load_dwordx4 v[192:195], v3, s[6:7] offset:3072
	s_add_i32 s63, s62, 0x1000
	s_and_b32 s63, s63, 0x3f000
	s_or_b32 s63, s63, s58
	v_or_b32_e32 v2, s63, v231
	global_load_dwordx4 v[174:177], v2, s[6:7] offset:2048
	global_load_dwordx4 v[178:181], v2, s[6:7] offset:3072
	v_pk_mul_f32 v[248:249], v[0:1], v[64:65] op_sel_hi:[0,1]
	v_pk_mul_f32 v[250:251], v[0:1], v[66:67] op_sel_hi:[0,1]
	ds_write_b128 v238, v[248:251]
	v_pk_mul_f32 v[248:249], v[0:1], v[68:69] op_sel_hi:[0,1]
	v_pk_mul_f32 v[250:251], v[0:1], v[74:75] op_sel_hi:[0,1]
	ds_write_b128 v238, v[248:251] offset:32
	v_pk_mul_f32 v[248:249], v[0:1], v[72:73] op_sel_hi:[0,1]
	v_pk_mul_f32 v[250:251], v[0:1], v[104:105] op_sel_hi:[0,1]
	ds_write_b128 v238, v[248:251] offset:64
	v_pk_mul_f32 v[248:249], v[0:1], v[106:107] op_sel_hi:[0,1]
	v_pk_mul_f32 v[250:251], v[0:1], v[172:173] op_sel_hi:[0,1]
	ds_write_b128 v238, v[248:251] offset:96
	v_pk_mul_f32 v[248:249], v[0:1], v[170:171] op_sel_hi:[0,1]
	v_pk_mul_f32 v[250:251], v[0:1], v[188:189] op_sel_hi:[0,1]
	ds_write_b128 v238, v[248:251] offset:128
	v_pk_mul_f32 v[248:249], v[0:1], v[190:191] op_sel_hi:[0,1]
	v_pk_mul_f32 v[250:251], v[0:1], v[202:203] op_sel_hi:[0,1]
	ds_write_b128 v238, v[248:251] offset:160
	v_pk_mul_f32 v[248:249], v[0:1], v[200:201] op_sel_hi:[0,1]
	v_pk_mul_f32 v[250:251], v[0:1], v[214:215] op_sel_hi:[0,1]
	ds_write_b128 v238, v[248:251] offset:192
	v_pk_mul_f32 v[248:249], v[0:1], v[216:217] op_sel_hi:[0,1]
	v_pk_mul_f32 v[250:251], v[0:1], v[222:223] op_sel_hi:[0,1]
	ds_write_b128 v238, v[248:251] offset:224
	v_add_u32_e32 v252, 0x200, v253
	v_and_or_b32 v2, v252, s54, v1
	ds_read_b128 v[248:251], v246
	ds_read_b128 v[160:163], v246 offset:1088
	s_waitcnt lgkmcnt(1)
	global_store_dwordx4 v2, v[248:251], s[10:11] nt
	s_nop 0
	ds_read_b128 v[248:251], v246 offset:2176
	v_or_b32_e32 v3, 0x8000, v2
	s_waitcnt lgkmcnt(1)
	global_store_dwordx4 v3, v[160:163], s[10:11] nt
	s_nop 0
	ds_read_b128 v[160:163], v246 offset:3264
	v_or_b32_e32 v252, 0x10000, v2
	s_waitcnt lgkmcnt(1)
	global_store_dwordx4 v252, v[248:251], s[10:11] nt
	s_nop 0
	ds_read_b128 v[248:251], v246 offset:4352
	v_or_b32_e32 v3, 0x18000, v2
	s_waitcnt lgkmcnt(1)
	global_store_dwordx4 v3, v[160:163], s[10:11] nt
	s_nop 0
	ds_read_b128 v[160:163], v246 offset:5440
	v_or_b32_e32 v252, 0x20000, v2
	s_waitcnt lgkmcnt(1)
	global_store_dwordx4 v252, v[248:251], s[10:11] nt
	s_nop 0
	ds_read_b128 v[248:251], v246 offset:6528
	v_or_b32_e32 v3, 0x28000, v2
	s_waitcnt lgkmcnt(1)
	global_store_dwordx4 v3, v[160:163], s[10:11] nt
	s_nop 0
	ds_read_b128 v[160:163], v246 offset:7616
	v_or_b32_e32 v252, 0x30000, v2
	s_waitcnt lgkmcnt(1)
	global_store_dwordx4 v252, v[248:251], s[10:11] nt
	v_or_b32_e32 v3, 0x38000, v2
	s_waitcnt lgkmcnt(0)
	global_store_dwordx4 v3, v[160:163], s[10:11] nt
	v_pk_mul_f32 v[248:249], v[0:1], v[70:71] op_sel_hi:[0,1]
	v_pk_mul_f32 v[250:251], v[0:1], v[76:77] op_sel_hi:[0,1]
	ds_write_b128 v238, v[248:251]
	v_pk_mul_f32 v[248:249], v[0:1], v[78:79] op_sel_hi:[0,1]
	v_pk_mul_f32 v[250:251], v[0:1], v[168:169] op_sel_hi:[0,1]
	ds_write_b128 v238, v[248:251] offset:32
	v_pk_mul_f32 v[248:249], v[0:1], v[126:127] op_sel_hi:[0,1]
	v_pk_mul_f32 v[250:251], v[0:1], v[184:185] op_sel_hi:[0,1]
	ds_write_b128 v238, v[248:251] offset:64
	v_pk_mul_f32 v[248:249], v[0:1], v[186:187] op_sel_hi:[0,1]
	v_pk_mul_f32 v[250:251], v[0:1], v[198:199] op_sel_hi:[0,1]
	ds_write_b128 v238, v[248:251] offset:96
	v_pk_mul_f32 v[248:249], v[0:1], v[196:197] op_sel_hi:[0,1]
	v_pk_mul_f32 v[250:251], v[0:1], v[210:211] op_sel_hi:[0,1]
	ds_write_b128 v238, v[248:251] offset:128
	v_pk_mul_f32 v[248:249], v[0:1], v[212:213] op_sel_hi:[0,1]
	v_pk_mul_f32 v[250:251], v[0:1], v[220:221] op_sel_hi:[0,1]
	ds_write_b128 v238, v[248:251] offset:160
	v_pk_mul_f32 v[248:249], v[0:1], v[218:219] op_sel_hi:[0,1]
	v_pk_mul_f32 v[250:251], v[0:1], v[224:225] op_sel_hi:[0,1]
	ds_write_b128 v238, v[248:251] offset:192
	v_pk_mul_f32 v[248:249], v[0:1], v[226:227] op_sel_hi:[0,1]
	v_pk_mul_f32 v[250:251], v[0:1], v[228:229] op_sel_hi:[0,1]
	ds_write_b128 v238, v[248:251] offset:224
	v_add_u32_e32 v252, 0x300, v253
	v_and_or_b32 v196, v252, s54, v1
	s_mov_b32 s72, s55
	s_mov_b32 s73, s56
	s_cmp_lt_u32 s31, 0x200
	s_cbranch_scc1 .Ltail_end
	s_waitcnt lgkmcnt(0)
	s_add_i32 s75, s12, 4
	v_mov_b32_e32 v248, s74
	v_mov_b32_e32 v249, s75
	ds_write_b32 v248, v249
.Ltail_end:
	s_mov_b32 s57, s24
	s_add_i32 s12, s12, 4
	s_cmp_eq_u32 s12, 32
	s_cbranch_scc1 .LBB1_22
.LBB1_14:
	s_and_b32 s24, s12, 24
	s_or_b32 s56, s24, s27
	s_and_b32 s24, s57, 1
	s_or_b32 s55, s24, s28
	s_add_i32 s24, s55, s29
	s_lshl_b32 s24, s24, 12
	s_lshl_b32 s58, s56, 18
	ds_read_b128 v[64:67], v243
	ds_read_b128 v[68:71], v243 offset:16
	s_waitcnt lgkmcnt(1)
	v_pk_mul_f32 v[76:77], v[64:65], s[22:23] op_sel_hi:[1,0]
	s_waitcnt lgkmcnt(0)
	v_pk_mul_f32 v[64:65], v[68:69], s[22:23] op_sel_hi:[1,0]
	v_pk_mul_f32 v[78:79], v[66:67], s[22:23] op_sel_hi:[1,0]
	v_pk_mul_f32 v[74:75], v[70:71], s[22:23] op_sel_hi:[1,0]
	v_cvt_pk_f16_f32 v204, v64, v65
	ds_read_b128 v[64:67], v243 offset:64
	ds_read_b128 v[68:71], v243 offset:80
	v_cvt_pk_f16_f32 v202, v76, v77
	v_cvt_pk_f16_f32 v205, v74, v75
	v_cvt_pk_f16_f32 v203, v78, v79
	s_waitcnt lgkmcnt(1)
	v_pk_mul_f32 v[76:77], v[64:65], s[22:23] op_sel_hi:[1,0]
	s_waitcnt lgkmcnt(0)
	v_pk_mul_f32 v[64:65], v[68:69], s[22:23] op_sel_hi:[1,0]
	v_pk_mul_f32 v[78:79], v[66:67], s[22:23] op_sel_hi:[1,0]
	v_pk_mul_f32 v[74:75], v[70:71], s[22:23] op_sel_hi:[1,0]
	v_cvt_pk_f16_f32 v208, v64, v65
	ds_read_b128 v[64:67], v243 offset:128
	ds_read_b128 v[68:71], v243 offset:144
	v_cvt_pk_f16_f32 v206, v76, v77
	v_cvt_pk_f16_f32 v209, v74, v75
	v_cvt_pk_f16_f32 v207, v78, v79
	s_waitcnt lgkmcnt(1)
	v_pk_mul_f32 v[76:77], v[64:65], s[22:23] op_sel_hi:[1,0]
	s_waitcnt lgkmcnt(0)
	v_pk_mul_f32 v[64:65], v[68:69], s[22:23] op_sel_hi:[1,0]
	v_pk_mul_f32 v[78:79], v[66:67], s[22:23] op_sel_hi:[1,0]
	v_pk_mul_f32 v[74:75], v[70:71], s[22:23] op_sel_hi:[1,0]
	v_cvt_pk_f16_f32 v212, v64, v65
	ds_read_b128 v[64:67], v243 offset:192
	ds_read_b128 v[68:71], v243 offset:208
	v_cvt_pk_f16_f32 v211, v78, v79
	v_cvt_pk_f16_f32 v210, v76, v77
	v_cvt_pk_f16_f32 v213, v74, v75
	s_waitcnt lgkmcnt(1)
	v_pk_mul_f32 v[78:79], v[66:67], s[22:23] op_sel_hi:[1,0]
	s_waitcnt lgkmcnt(0)
	v_pk_mul_f32 v[66:67], v[70:71], s[22:23] op_sel_hi:[1,0]
	v_pk_mul_f32 v[64:65], v[64:65], s[22:23] op_sel_hi:[1,0]
	v_pk_mul_f32 v[68:69], v[68:69], s[22:23] op_sel_hi:[1,0]
	v_cvt_pk_f16_f32 v214, v64, v65
	v_cvt_pk_f16_f32 v216, v68, v69
	v_cvt_pk_f16_f32 v217, v66, v67
	v_cvt_pk_f16_f32 v215, v78, v79
	s_waitcnt vmcnt(57)
	v_mfma_f32_32x32x16_f16 v[112:127], v[48:51], v[202:205], 0
	s_waitcnt vmcnt(56)
	v_mfma_f32_32x32x16_f16 v[112:127], v[52:55], v[206:209], v[112:127]
	s_waitcnt vmcnt(55)
	v_mfma_f32_32x32x16_f16 v[112:127], v[56:59], v[210:213], v[112:127]
	s_waitcnt vmcnt(54)
	v_mfma_f32_32x32x16_f16 v[112:127], v[60:63], v[214:217], v[112:127]
	s_waitcnt vmcnt(42)
	v_mfma_f32_32x32x16_f16 v[48:63], v[32:35], v[202:205], 0
	s_waitcnt vmcnt(41)
	v_mfma_f32_32x32x16_f16 v[48:63], v[36:39], v[206:209], v[48:63]
	v_mfma_f32_32x32x16_f16 v[48:63], v[40:43], v[210:213], v[48:63]
	v_mfma_f32_32x32x16_f16 v[48:63], v[44:47], v[214:217], v[48:63]
	s_waitcnt vmcnt(40)
	v_mfma_f32_32x32x16_f16 v[32:47], v[16:19], v[202:205], 0
	s_waitcnt vmcnt(39)
	v_mfma_f32_32x32x16_f16 v[32:47], v[20:23], v[206:209], v[32:47]
	s_waitcnt vmcnt(38)
	v_mfma_f32_32x32x16_f16 v[32:47], v[24:27], v[210:213], v[32:47]
	s_waitcnt vmcnt(37)
	v_mfma_f32_32x32x16_f16 v[32:47], v[28:31], v[214:217], v[32:47]
	s_waitcnt vmcnt(36)
	v_mfma_f32_32x32x16_f16 v[16:31], v[4:7], v[202:205], 0
	s_waitcnt vmcnt(35)
	v_mfma_f32_32x32x16_f16 v[16:31], v[8:11], v[206:209], v[16:31]
	s_waitcnt vmcnt(34)
	v_mfma_f32_32x32x16_f16 v[16:31], v[12:15], v[210:213], v[16:31]
	v_mfma_f32_32x32x16_f16 v[16:31], v[148:151], v[214:217], v[16:31]
	v_mfma_f32_32x32x16_f16 v[0:15], v[132:135], v[202:205], 0
	v_mfma_f32_32x32x16_f16 v[0:15], v[136:139], v[206:209], v[0:15]
	v_mfma_f32_32x32x16_f16 v[0:15], v[140:143], v[210:213], v[0:15]
	v_mfma_f32_32x32x16_f16 v[0:15], v[144:147], v[214:217], v[0:15]
	s_waitcnt vmcnt(17)
	v_mfma_f32_32x32x16_f16 v[64:79], v[80:83], v[202:205], 0
	s_waitcnt vmcnt(16)
	v_mfma_f32_32x32x16_f16 v[64:79], v[84:87], v[206:209], v[64:79]
	s_waitcnt vmcnt(15)
	v_mfma_f32_32x32x16_f16 v[64:79], v[88:91], v[210:213], v[64:79]
	s_waitcnt vmcnt(14)
	v_mfma_f32_32x32x16_f16 v[64:79], v[92:95], v[214:217], v[64:79]
	s_waitcnt vmcnt(13)
	v_mfma_f32_32x32x16_f16 v[80:95], v[96:99], v[202:205], 0
	s_waitcnt vmcnt(12)
	v_mfma_f32_32x32x16_f16 v[80:95], v[100:103], v[206:209], v[80:95]
	s_waitcnt vmcnt(11)
	v_mfma_f32_32x32x16_f16 v[80:95], v[108:111], v[210:213], v[80:95]
	s_waitcnt vmcnt(10)
	v_mfma_f32_32x32x16_f16 v[80:95], v[192:195], v[214:217], v[80:95]
	v_mfma_f32_32x32x16_f16 v[96:111], v[152:155], v[202:205], 0
	v_mfma_f32_32x32x16_f16 v[96:111], v[156:159], v[206:209], v[96:111]
	s_waitcnt vmcnt(9)
	v_mfma_f32_32x32x16_f16 v[96:111], v[174:177], v[210:213], v[96:111]
	s_waitcnt vmcnt(8)
	v_mfma_f32_32x32x16_f16 v[96:111], v[178:181], v[214:217], v[96:111]
	s_and_b32 s25, s24, 0x3f000
	s_addk_i32 s24, 0x1000
	s_or_b32 s25, s58, s25
	s_and_b32 s24, s24, 0x3f000
	v_or_b32_e32 v132, s25, v231
	s_or_b32 s24, s58, s24
	global_load_dwordx4 v[156:159], v132, s[16:17]
	global_load_dwordx4 v[160:163], v132, s[16:17] offset:1024
	global_load_dwordx4 v[152:155], v132, s[16:17] offset:2048
	global_load_dwordx4 v[148:151], v132, s[16:17] offset:3072
	v_or_b32_e32 v132, s24, v231
	global_load_dwordx4 v[144:147], v132, s[16:17]
	global_load_dwordx4 v[140:143], v132, s[16:17] offset:1024
	global_load_dwordx4 v[136:139], v132, s[16:17] offset:2048
	s_nop 0
	global_load_dwordx4 v[132:135], v132, s[16:17] offset:3072
	v_max_f32_e32 v166, v113, v113
	v_max_f32_e32 v167, v112, v112
	v_max_f32_e32 v166, v167, v166
	v_max3_f32 v166, v166, v114, v115
	v_max3_f32 v166, v166, v116, v117
	v_max3_f32 v166, v166, v118, v119
	v_max3_f32 v166, v166, v120, v121
	v_max3_f32 v166, v166, v122, v123
	v_max3_f32 v166, v166, v124, v125
	v_max3_f32 v166, v166, v126, v127
	v_max3_f32 v166, v166, v96, v97
	v_max3_f32 v166, v166, v98, v99
	v_max3_f32 v166, v166, v100, v101
	v_max3_f32 v166, v166, v102, v103
	v_max3_f32 v166, v166, v104, v105
	v_max3_f32 v166, v166, v106, v107
	v_max3_f32 v166, v166, v108, v109
	v_max3_f32 v166, v166, v110, v111
	v_max3_f32 v166, v166, v80, v81
	v_max3_f32 v166, v166, v82, v83
	v_max3_f32 v166, v166, v84, v85
	v_max3_f32 v166, v166, v86, v87
	v_max3_f32 v166, v166, v88, v89
	v_max3_f32 v166, v166, v90, v91
	v_max3_f32 v166, v166, v92, v93
	v_max3_f32 v166, v166, v94, v95
	v_max3_f32 v166, v166, v64, v65
	v_max3_f32 v166, v166, v66, v67
	v_max3_f32 v166, v166, v68, v69
	v_max3_f32 v166, v166, v70, v71
	v_max3_f32 v166, v166, v72, v73
	v_max3_f32 v166, v166, v74, v75
	v_max3_f32 v166, v166, v76, v77
	v_max3_f32 v166, v166, v78, v79
	v_max3_f32 v166, v166, v48, v49
	v_max3_f32 v166, v166, v50, v51
	v_max3_f32 v166, v166, v52, v53
	v_max3_f32 v166, v166, v54, v55
	v_max3_f32 v166, v166, v56, v57
	v_max3_f32 v166, v166, v58, v59
	v_max3_f32 v166, v166, v60, v61
	v_max3_f32 v166, v166, v62, v63
	v_max3_f32 v166, v166, v32, v33
	v_max3_f32 v166, v166, v34, v35
	v_max3_f32 v166, v166, v36, v37
	v_max3_f32 v166, v166, v38, v39
	v_max3_f32 v166, v166, v40, v41
	v_max3_f32 v166, v166, v42, v43
	v_max3_f32 v166, v166, v44, v45
	v_max3_f32 v166, v166, v46, v47
	v_max3_f32 v166, v166, v16, v17
	v_max3_f32 v166, v166, v18, v19
	v_max3_f32 v166, v166, v20, v21
	v_max3_f32 v166, v166, v22, v23
	v_max3_f32 v166, v166, v24, v25
	v_max3_f32 v166, v166, v26, v27
	v_max3_f32 v166, v166, v28, v29
	v_max3_f32 v166, v166, v30, v31
	v_max3_f32 v166, v166, v0, v1
	v_max3_f32 v166, v166, v2, v3
	v_max3_f32 v166, v166, v4, v5
	v_max3_f32 v166, v166, v6, v7
	v_max3_f32 v166, v166, v8, v9
	v_max3_f32 v166, v166, v10, v11
	v_max3_f32 v166, v166, v12, v13
	v_max3_f32 v166, v166, v14, v15
	ds_bpermute_b32 v167, v234, v166
	s_waitcnt lgkmcnt(0)
	v_max_f32_e32 v167, v167, v167
	v_max_f32_e32 v247, v166, v167
	s_and_saveexec_b64 s[24:25], s[0:1]
	v_add_u32_e32 v166, s31, v235
	ds_write_b32 v166, v247
	s_or_b64 exec, exec, s[24:25]
	v_sub_f32_e32 v112, v112, v247
	v_exp_f32_e32 v208, v112
	v_sub_f32_e32 v112, v113, v247
	v_exp_f32_e32 v209, v112
	v_sub_f32_e32 v112, v114, v247
	v_exp_f32_e32 v204, v112
	v_sub_f32_e32 v112, v115, v247
	v_exp_f32_e32 v205, v112
	v_sub_f32_e32 v113, v116, v247
	v_add_f32_e32 v112, 0, v208
	v_exp_f32_e32 v182, v113
	v_sub_f32_e32 v113, v117, v247
	v_add_f32_e32 v112, v112, v209
	v_exp_f32_e32 v183, v113
	v_sub_f32_e32 v113, v118, v247
	v_add_f32_e32 v112, v112, v204
	v_exp_f32_e32 v178, v113
	v_sub_f32_e32 v113, v119, v247
	v_add_f32_e32 v112, v112, v205
	v_exp_f32_e32 v179, v113
	v_sub_f32_e32 v113, v120, v247
	v_add_f32_e32 v112, v112, v182
	v_exp_f32_e32 v166, v113
	v_sub_f32_e32 v113, v121, v247
	v_add_f32_e32 v112, v112, v183
	v_exp_f32_e32 v167, v113
	v_sub_f32_e32 v113, v122, v247
	v_add_f32_e32 v112, v112, v178
	v_exp_f32_e32 v118, v113
	v_sub_f32_e32 v113, v123, v247
	v_add_f32_e32 v112, v112, v179
	v_exp_f32_e32 v119, v113
	v_sub_f32_e32 v113, v124, v247
	v_add_f32_e32 v112, v112, v166
	v_exp_f32_e32 v116, v113
	v_sub_f32_e32 v113, v125, v247
	v_add_f32_e32 v112, v112, v167
	v_exp_f32_e32 v117, v113
	v_sub_f32_e32 v113, v126, v247
	v_add_f32_e32 v112, v112, v118
	v_exp_f32_e32 v114, v113
	v_sub_f32_e32 v113, v127, v247
	v_add_f32_e32 v112, v112, v119
	v_exp_f32_e32 v115, v113
	v_add_f32_e32 v112, v112, v116
	v_add_f32_e32 v112, v112, v117
	v_add_f32_e32 v112, v112, v114
	v_sub_f32_e32 v96, v96, v247
	v_add_f32_e32 v120, v112, v115
	v_exp_f32_e32 v112, v96
	v_sub_f32_e32 v96, v97, v247
	v_exp_f32_e32 v113, v96
	v_sub_f32_e32 v96, v98, v247
	v_exp_f32_e32 v98, v96
	v_sub_f32_e32 v96, v99, v247
	v_exp_f32_e32 v99, v96
	v_sub_f32_e32 v97, v100, v247
	v_add_f32_e32 v96, v120, v112
	v_exp_f32_e32 v100, v97
	v_sub_f32_e32 v97, v101, v247
	v_add_f32_e32 v96, v96, v113
	v_exp_f32_e32 v101, v97
	v_sub_f32_e32 v97, v102, v247
	v_add_f32_e32 v96, v96, v98
	v_exp_f32_e32 v120, v97
	v_sub_f32_e32 v97, v103, v247
	v_add_f32_e32 v96, v96, v99
	v_exp_f32_e32 v121, v97
	v_sub_f32_e32 v97, v104, v247
	v_add_f32_e32 v96, v96, v100
	v_exp_f32_e32 v102, v97
	v_sub_f32_e32 v97, v105, v247
	v_add_f32_e32 v96, v96, v101
	v_exp_f32_e32 v103, v97
	v_sub_f32_e32 v97, v106, v247
	v_add_f32_e32 v96, v96, v120
	v_exp_f32_e32 v122, v97
	v_sub_f32_e32 v97, v107, v247
	v_add_f32_e32 v96, v96, v121
	v_exp_f32_e32 v123, v97
	v_sub_f32_e32 v97, v108, v247
	v_add_f32_e32 v96, v96, v102
	v_exp_f32_e32 v124, v97
	v_sub_f32_e32 v97, v109, v247
	v_add_f32_e32 v96, v96, v103
	v_exp_f32_e32 v125, v97
	v_sub_f32_e32 v97, v110, v247
	v_add_f32_e32 v96, v96, v122
	v_exp_f32_e32 v180, v97
	v_sub_f32_e32 v97, v111, v247
	v_add_f32_e32 v96, v96, v123
	v_exp_f32_e32 v181, v97
	v_sub_f32_e32 v80, v80, v247
	v_add_f32_e32 v96, v96, v124
	v_exp_f32_e32 v80, v80
	v_sub_f32_e32 v81, v81, v247
	v_add_f32_e32 v96, v96, v125
	v_exp_f32_e32 v81, v81
	v_sub_f32_e32 v82, v82, v247
	v_add_f32_e32 v96, v96, v180
	v_exp_f32_e32 v82, v82
	v_sub_f32_e32 v83, v83, v247
	v_add_f32_e32 v96, v96, v181
	v_exp_f32_e32 v83, v83
	v_add_f32_e32 v96, v96, v80
	v_sub_f32_e32 v84, v84, v247
	v_add_f32_e32 v96, v96, v81
	v_exp_f32_e32 v84, v84
	v_sub_f32_e32 v85, v85, v247
	v_add_f32_e32 v96, v96, v82
	v_exp_f32_e32 v85, v85
	v_sub_f32_e32 v86, v86, v247
	v_add_f32_e32 v104, v96, v83
	v_exp_f32_e32 v96, v86
	v_sub_f32_e32 v86, v87, v247
	v_exp_f32_e32 v97, v86
	v_add_f32_e32 v86, v104, v84
	v_add_f32_e32 v86, v86, v85
	v_add_f32_e32 v86, v86, v96
	v_add_f32_e32 v104, v86, v97
	v_sub_f32_e32 v86, v88, v247
	v_exp_f32_e32 v86, v86
	v_sub_f32_e32 v87, v89, v247
	v_exp_f32_e32 v87, v87
	v_sub_f32_e32 v88, v90, v247
	v_exp_f32_e32 v88, v88
	v_sub_f32_e32 v89, v91, v247
	v_exp_f32_e32 v89, v89
	v_add_f32_e32 v90, v104, v86
	v_add_f32_e32 v90, v90, v87
	v_add_f32_e32 v90, v90, v88
	v_add_f32_e32 v104, v90, v89
	v_sub_f32_e32 v90, v92, v247
	v_exp_f32_e32 v90, v90
	v_sub_f32_e32 v91, v93, v247
	v_exp_f32_e32 v91, v91
	v_sub_f32_e32 v92, v94, v247
	v_exp_f32_e32 v94, v92
	v_sub_f32_e32 v92, v95, v247
	v_exp_f32_e32 v95, v92
	v_add_f32_e32 v92, v104, v90
	v_add_f32_e32 v92, v92, v91
	v_add_f32_e32 v92, v92, v94
	v_sub_f32_e32 v64, v64, v247
	v_add_f32_e32 v104, v92, v95
	v_exp_f32_e32 v92, v64
	v_sub_f32_e32 v64, v65, v247
	v_exp_f32_e32 v93, v64
	v_sub_f32_e32 v64, v66, v247
	v_exp_f32_e32 v108, v64
	v_sub_f32_e32 v64, v67, v247
	v_exp_f32_e32 v109, v64
	v_sub_f32_e32 v65, v68, v247
	v_add_f32_e32 v64, v104, v92
	v_exp_f32_e32 v110, v65
	v_sub_f32_e32 v65, v69, v247
	v_add_f32_e32 v64, v64, v93
	v_exp_f32_e32 v111, v65
	v_sub_f32_e32 v65, v70, v247
	v_add_f32_e32 v64, v64, v108
	v_exp_f32_e32 v176, v65
	v_sub_f32_e32 v65, v71, v247
	v_add_f32_e32 v64, v64, v109
	v_exp_f32_e32 v177, v65
	v_sub_f32_e32 v65, v72, v247
	v_add_f32_e32 v64, v64, v110
	v_exp_f32_e32 v174, v65
	v_sub_f32_e32 v65, v73, v247
	v_add_f32_e32 v64, v64, v111
	v_exp_f32_e32 v175, v65
	v_sub_f32_e32 v65, v74, v247
	v_add_f32_e32 v64, v64, v176
	v_exp_f32_e32 v192, v65
	v_sub_f32_e32 v65, v75, v247
	v_add_f32_e32 v64, v64, v177
	v_exp_f32_e32 v193, v65
	v_sub_f32_e32 v65, v76, v247
	v_add_f32_e32 v64, v64, v174
	v_exp_f32_e32 v194, v65
	v_sub_f32_e32 v65, v77, v247
	v_add_f32_e32 v64, v64, v175
	v_exp_f32_e32 v195, v65
	v_sub_f32_e32 v65, v78, v247
	v_add_f32_e32 v64, v64, v192
	v_exp_f32_e32 v206, v65
	v_sub_f32_e32 v65, v79, v247
	v_add_f32_e32 v64, v64, v193
	v_exp_f32_e32 v207, v65
	v_add_f32_e32 v64, v64, v194
	v_add_f32_e32 v64, v64, v195
	v_add_f32_e32 v64, v64, v206
	v_sub_f32_e32 v48, v48, v247
	v_add_f32_e32 v68, v64, v207
	v_exp_f32_e32 v64, v48
	v_sub_f32_e32 v48, v49, v247
	v_exp_f32_e32 v65, v48
	v_sub_f32_e32 v48, v50, v247
	v_exp_f32_e32 v66, v48
	v_sub_f32_e32 v48, v51, v247
	v_exp_f32_e32 v67, v48
	v_sub_f32_e32 v49, v52, v247
	v_add_f32_e32 v48, v68, v64
	v_exp_f32_e32 v68, v49
	v_sub_f32_e32 v49, v53, v247
	v_add_f32_e32 v48, v48, v65
	v_exp_f32_e32 v69, v49
	v_sub_f32_e32 v49, v54, v247
	v_add_f32_e32 v48, v48, v66
	v_exp_f32_e32 v74, v49
	v_sub_f32_e32 v49, v55, v247
	v_add_f32_e32 v48, v48, v67
	v_exp_f32_e32 v75, v49
	v_sub_f32_e32 v49, v56, v247
	v_add_f32_e32 v48, v48, v68
	v_exp_f32_e32 v72, v49
	v_sub_f32_e32 v49, v57, v247
	v_add_f32_e32 v48, v48, v69
	v_exp_f32_e32 v73, v49
	v_sub_f32_e32 v49, v58, v247
	v_add_f32_e32 v48, v48, v74
	v_exp_f32_e32 v104, v49
	v_sub_f32_e32 v49, v59, v247
	v_add_f32_e32 v48, v48, v75
	v_exp_f32_e32 v105, v49
	v_sub_f32_e32 v49, v60, v247
	v_add_f32_e32 v48, v48, v72
	v_exp_f32_e32 v106, v49
	v_sub_f32_e32 v49, v61, v247
	v_add_f32_e32 v48, v48, v73
	v_exp_f32_e32 v107, v49
	v_sub_f32_e32 v49, v62, v247
	v_add_f32_e32 v48, v48, v104
	v_exp_f32_e32 v172, v49
	v_sub_f32_e32 v49, v63, v247
	v_add_f32_e32 v48, v48, v105
	v_exp_f32_e32 v173, v49
	v_sub_f32_e32 v32, v32, v247
	v_add_f32_e32 v48, v48, v106
	v_exp_f32_e32 v170, v32
	v_sub_f32_e32 v32, v33, v247
	v_add_f32_e32 v48, v48, v107
	v_exp_f32_e32 v171, v32
	v_sub_f32_e32 v32, v34, v247
	v_add_f32_e32 v48, v48, v172
	v_exp_f32_e32 v188, v32
	v_sub_f32_e32 v32, v35, v247
	v_add_f32_e32 v48, v48, v173
	v_exp_f32_e32 v189, v32
	v_sub_f32_e32 v33, v36, v247
	v_add_f32_e32 v32, v48, v170
	v_exp_f32_e32 v190, v33
	v_sub_f32_e32 v33, v37, v247
	v_add_f32_e32 v32, v32, v171
	v_exp_f32_e32 v191, v33
	v_sub_f32_e32 v33, v38, v247
	v_add_f32_e32 v32, v32, v188
	v_exp_f32_e32 v202, v33
	v_sub_f32_e32 v33, v39, v247
	v_add_f32_e32 v32, v32, v189
	v_exp_f32_e32 v203, v33
	v_sub_f32_e32 v33, v40, v247
	v_add_f32_e32 v32, v32, v190
	v_exp_f32_e32 v200, v33
	v_sub_f32_e32 v33, v41, v247
	v_add_f32_e32 v32, v32, v191
	v_exp_f32_e32 v201, v33
	v_sub_f32_e32 v33, v42, v247
	v_add_f32_e32 v32, v32, v202
	v_exp_f32_e32 v214, v33
	v_sub_f32_e32 v33, v43, v247
	v_add_f32_e32 v32, v32, v203
	v_exp_f32_e32 v215, v33
	v_sub_f32_e32 v33, v44, v247
	v_add_f32_e32 v32, v32, v200
	v_exp_f32_e32 v216, v33
	v_sub_f32_e32 v33, v45, v247
	v_add_f32_e32 v32, v32, v201
	v_exp_f32_e32 v217, v33
	v_sub_f32_e32 v33, v46, v247
	v_add_f32_e32 v32, v32, v214
	v_exp_f32_e32 v222, v33
	v_sub_f32_e32 v33, v47, v247
	v_add_f32_e32 v32, v32, v215
	v_exp_f32_e32 v223, v33
	v_sub_f32_e32 v16, v16, v247
	v_add_f32_e32 v32, v32, v216
	v_exp_f32_e32 v70, v16
	v_sub_f32_e32 v16, v17, v247
	v_add_f32_e32 v32, v32, v217
	v_exp_f32_e32 v71, v16
	v_sub_f32_e32 v16, v18, v247
	v_add_f32_e32 v32, v32, v222
	v_exp_f32_e32 v76, v16
	v_sub_f32_e32 v16, v19, v247
	v_add_f32_e32 v32, v32, v223
	v_exp_f32_e32 v77, v16
	v_sub_f32_e32 v17, v20, v247
	v_add_f32_e32 v16, v32, v70
	v_exp_f32_e32 v78, v17
	v_sub_f32_e32 v17, v21, v247
	v_add_f32_e32 v16, v16, v71
	v_exp_f32_e32 v79, v17
	v_sub_f32_e32 v17, v22, v247
	v_add_f32_e32 v16, v16, v76
	v_exp_f32_e32 v168, v17
	v_sub_f32_e32 v17, v23, v247
	v_add_f32_e32 v16, v16, v77
	v_exp_f32_e32 v169, v17
	v_sub_f32_e32 v17, v24, v247
	v_add_f32_e32 v16, v16, v78
	v_exp_f32_e32 v126, v17
	v_sub_f32_e32 v17, v25, v247
	v_add_f32_e32 v16, v16, v79
	v_exp_f32_e32 v127, v17
	v_sub_f32_e32 v17, v26, v247
	v_add_f32_e32 v16, v16, v168
	v_exp_f32_e32 v184, v17
	v_sub_f32_e32 v17, v27, v247
	v_add_f32_e32 v16, v16, v169
	v_exp_f32_e32 v185, v17
	v_sub_f32_e32 v17, v28, v247
	v_add_f32_e32 v16, v16, v126
	v_exp_f32_e32 v186, v17
	v_sub_f32_e32 v17, v29, v247
	v_add_f32_e32 v16, v16, v127
	v_exp_f32_e32 v187, v17
	v_sub_f32_e32 v17, v30, v247
	v_add_f32_e32 v16, v16, v184
	v_exp_f32_e32 v198, v17
	v_sub_f32_e32 v17, v31, v247
	v_add_f32_e32 v16, v16, v185
	v_exp_f32_e32 v199, v17
	v_sub_f32_e32 v0, v0, v247
	v_add_f32_e32 v16, v16, v186
	v_exp_f32_e32 v196, v0
	v_sub_f32_e32 v0, v1, v247
	v_add_f32_e32 v16, v16, v187
	v_exp_f32_e32 v197, v0
	v_sub_f32_e32 v0, v2, v247
	v_add_f32_e32 v16, v16, v198
	v_exp_f32_e32 v210, v0
	v_sub_f32_e32 v0, v3, v247
	v_add_f32_e32 v16, v16, v199
	v_exp_f32_e32 v211, v0
	v_sub_f32_e32 v1, v4, v247
	v_add_f32_e32 v0, v16, v196
	v_exp_f32_e32 v212, v1
	v_sub_f32_e32 v1, v5, v247
	v_add_f32_e32 v0, v0, v197
	v_exp_f32_e32 v213, v1
	v_sub_f32_e32 v1, v6, v247
	v_add_f32_e32 v0, v0, v210
	v_exp_f32_e32 v220, v1
	v_sub_f32_e32 v1, v7, v247
	v_add_f32_e32 v0, v0, v211
	v_exp_f32_e32 v221, v1
	v_sub_f32_e32 v1, v8, v247
	v_add_f32_e32 v0, v0, v212
	v_exp_f32_e32 v218, v1
	v_sub_f32_e32 v1, v9, v247
	v_add_f32_e32 v0, v0, v213
	v_exp_f32_e32 v219, v1
	v_sub_f32_e32 v1, v10, v247
	v_add_f32_e32 v0, v0, v220
	v_exp_f32_e32 v224, v1
	v_sub_f32_e32 v1, v11, v247
	v_add_f32_e32 v0, v0, v221
	v_exp_f32_e32 v225, v1
	v_sub_f32_e32 v1, v12, v247
	v_add_f32_e32 v0, v0, v218
	v_exp_f32_e32 v226, v1
	v_sub_f32_e32 v1, v13, v247
	v_add_f32_e32 v0, v0, v219
	v_exp_f32_e32 v227, v1
	v_sub_f32_e32 v1, v14, v247
	v_add_f32_e32 v0, v0, v224
	v_exp_f32_e32 v228, v1
	v_sub_f32_e32 v1, v15, v247
	v_add_f32_e32 v0, v0, v225
	v_exp_f32_e32 v229, v1
	v_add_f32_e32 v0, v0, v226
	v_add_f32_e32 v0, v0, v227
	v_add_f32_e32 v0, v0, v228
	v_add_f32_e32 v0, v0, v229
	ds_bpermute_b32 v1, v234, v0
	s_and_saveexec_b64 s[24:25], s[0:1]
	s_cbranch_execz .LBB1_18
	s_waitcnt lgkmcnt(0)
	v_add_f32_e32 v0, v0, v1
	v_add_u32_e32 v1, s31, v236
	ds_write_b32 v1, v0

.LBB1_22:
	ds_read_b128 v[184:187], v246
	ds_read_b128 v[188:191], v246 offset:1088
	s_waitcnt lgkmcnt(1)
	global_store_dwordx4 v196, v[184:187], s[10:11] nt
	s_nop 0
	ds_read_b128 v[184:187], v246 offset:2176
	v_or_b32_e32 v197, 0x8000, v196
	s_waitcnt lgkmcnt(1)
	global_store_dwordx4 v197, v[188:191], s[10:11] nt
	s_nop 0
	ds_read_b128 v[188:191], v246 offset:3264
	v_or_b32_e32 v197, 0x10000, v196
	s_waitcnt lgkmcnt(1)
	global_store_dwordx4 v197, v[184:187], s[10:11] nt
	s_nop 0
	ds_read_b128 v[184:187], v246 offset:4352
	v_or_b32_e32 v197, 0x18000, v196
	s_waitcnt lgkmcnt(1)
	global_store_dwordx4 v197, v[188:191], s[10:11] nt
	s_nop 0
	ds_read_b128 v[188:191], v246 offset:5440
	v_or_b32_e32 v197, 0x20000, v196
	s_waitcnt lgkmcnt(1)
	global_store_dwordx4 v197, v[184:187], s[10:11] nt
	s_nop 0
	ds_read_b128 v[184:187], v246 offset:6528
	v_or_b32_e32 v197, 0x28000, v196
	s_waitcnt lgkmcnt(1)
	global_store_dwordx4 v197, v[188:191], s[10:11] nt
	s_nop 0
	ds_read_b128 v[188:191], v246 offset:7616
	v_or_b32_e32 v197, 0x30000, v196
	s_waitcnt lgkmcnt(1)
	global_store_dwordx4 v197, v[184:187], s[10:11] nt
	v_or_b32_e32 v197, 0x38000, v196
	s_waitcnt lgkmcnt(0)
	global_store_dwordx4 v197, v[188:191], s[10:11] nt

	.amdhsa_kernel _Z9attn_mainPKfPKDv8_DF16_S3_S0_PfS4_S4_
		.amdhsa_group_segment_fixed_size 158784
		.amdhsa_private_segment_fixed_size 0
		.amdhsa_kernarg_size 56
		.amdhsa_user_sgpr_count 2
		.amdhsa_user_sgpr_dispatch_ptr 0
		.amdhsa_user_sgpr_queue_ptr 0
		.amdhsa_user_sgpr_kernarg_segment_ptr 1
		.amdhsa_user_sgpr_dispatch_id 0
		.amdhsa_user_sgpr_kernarg_preload_length 0
		.amdhsa_user_sgpr_kernarg_preload_offset 0
		.amdhsa_user_sgpr_private_segment_size 0
		.amdhsa_uses_dynamic_stack 0
		.amdhsa_enable_private_segment 0
		.amdhsa_system_sgpr_workgroup_id_x 1
		.amdhsa_system_sgpr_workgroup_id_y 0
		.amdhsa_system_sgpr_workgroup_id_z 0
		.amdhsa_system_sgpr_workgroup_info 0
		.amdhsa_system_vgpr_workitem_id 0
		.amdhsa_next_free_vgpr 254
		.amdhsa_next_free_sgpr 96
		.amdhsa_accum_offset 256
		.amdhsa_reserve_vcc 1
		.amdhsa_float_round_mode_32 0
		.amdhsa_float_round_mode_16_64 0
		.amdhsa_float_denorm_mode_32 3
		.amdhsa_float_denorm_mode_16_64 3
		.amdhsa_dx10_clamp 1
		.amdhsa_ieee_mode 1
		.amdhsa_fp16_overflow 0
		.amdhsa_tg_split 0
		.amdhsa_exception_fp_ieee_invalid_op 0
		.amdhsa_exception_fp_denorm_src 0
		.amdhsa_exception_fp_ieee_div_zero 0
		.amdhsa_exception_fp_ieee_overflow 0
		.amdhsa_exception_fp_ieee_underflow 0
		.amdhsa_exception_fp_ieee_inexact 0
		.amdhsa_exception_int_div_zero 0
	.end_amdhsa_kernel

amdhsa.kernels:
  - .agpr_count:     0
    .args:
      - .actual_access:  read_only
        .address_space:  global
        .offset:         0
        .size:           8
        .value_kind:     global_buffer
      - .actual_access:  read_only
        .address_space:  global
        .offset:         8
        .size:           8
        .value_kind:     global_buffer
      - .actual_access:  write_only
        .address_space:  global
        .offset:         16
        .size:           8
        .value_kind:     global_buffer
      - .actual_access:  write_only
        .address_space:  global
        .offset:         24
        .size:           8
        .value_kind:     global_buffer
    .group_segment_fixed_size: 17408
    .kernarg_segment_align: 8
    .kernarg_segment_size: 32
    .language:       OpenCL C
    .language_version:
      - 2
      - 0
    .max_flat_workgroup_size: 256
    .name:           _Z7prep_kvPKfS0_PDv8_DF16_S2_
    .private_segment_fixed_size: 0
    .sgpr_count:     18
    .sgpr_spill_count: 0
    .symbol:         _Z7prep_kvPKfS0_PDv8_DF16_S2_.kd
    .uniform_work_group_size: 1
    .uses_dynamic_stack: false
    .vgpr_count:     31
    .vgpr_spill_count: 0
    .wavefront_size: 64
  - .agpr_count:     0
    .args:
      - .actual_access:  read_only
        .address_space:  global
        .offset:         0
        .size:           8
        .value_kind:     global_buffer
      - .actual_access:  read_only
        .address_space:  global
        .offset:         8
        .size:           8
        .value_kind:     global_buffer
      - .actual_access:  read_only
        .address_space:  global
        .offset:         16
        .size:           8
        .value_kind:     global_buffer
      - .actual_access:  read_only
        .address_space:  global
        .offset:         24
        .size:           8
        .value_kind:     global_buffer
      - .actual_access:  write_only
        .address_space:  global
        .offset:         32
        .size:           8
        .value_kind:     global_buffer
      - .actual_access:  write_only
        .address_space:  global
        .offset:         40
        .size:           8
        .value_kind:     global_buffer
      - .actual_access:  write_only
        .address_space:  global
        .offset:         48
        .size:           8
        .value_kind:     global_buffer
    .group_segment_fixed_size: 158784
    .kernarg_segment_align: 8
    .kernarg_segment_size: 56
    .language:       OpenCL C
    .language_version:
      - 2
      - 0
    .max_flat_workgroup_size: 512
    .name:           _Z9attn_mainPKfPKDv8_DF16_S3_S0_PfS4_S4_
    .private_segment_fixed_size: 0
    .sgpr_count:     68
    .sgpr_spill_count: 0
    .symbol:         _Z9attn_mainPKfPKDv8_DF16_S3_S0_PfS4_S4_.kd
    .uniform_work_group_size: 1
    .uses_dynamic_stack: false
    .vgpr_count:     254
    .vgpr_spill_count: 0
    .wavefront_size: 64
